# speedup vs baseline: 1.0006x; 1.0006x over previous
.Lmy_loopb:
	ds_read_b128 v[158:161], v248 offset:0
	ds_read_b128 v[162:165], v248 offset:1024
	ds_read_b128 v[166:169], v249 offset:2048
	ds_read_b128 v[170:173], v249 offset:3072
	v_mfma_f32_16x16x32_f16 v[218:221], v[82:85], v[150:153], v[106:109]
	v_mfma_f32_16x16x32_f16 v[222:225], v[90:93], v[150:153], v[110:113]
	v_mfma_f32_16x16x32_f16 v[218:221], v[86:89], v[154:157], v[218:221]
	v_mfma_f32_16x16x32_f16 v[222:225], v[94:97], v[154:157], v[222:225]
	s_waitcnt lgkmcnt(2)
	v_mfma_f32_16x16x32_f16 v[210:213], v[54:57], v[158:161], v[210:213]
	v_mfma_f32_16x16x32_f16 v[210:213], v[58:61], v[162:165], v[210:213]
	s_waitcnt lgkmcnt(0)
	v_mfma_f32_16x16x32_f16 v[210:213], v[62:65], v[166:169], v[210:213]
	v_mfma_f32_16x16x32_f16 v[210:213], v[50:53], v[170:173], v[210:213]
	s_waitcnt vmcnt(9)
	v_cvt_pk_f16_f32 v251, v192, v193
	ds_write_b32 v1, v251 offset:0
	ds_read_b128 v[150:153], v186 offset:6144
	ds_read_b128 v[154:157], v186 offset:7168
	s_nop 2
	v_exp_f32_e32 v226, v210
	v_exp_f32_e32 v227, v211
	v_mfma_f32_16x16x32_f16 v[214:217], v[34:37], v[158:161], v[214:217]
	v_min_f32_e32 v228, s42, v212
	v_exp_f32_e32 v229, v213
	v_mfma_f32_16x16x32_f16 v[214:217], v[38:41], v[162:165], v[214:217]
	v_exp_f32_e32 v228, v228
	v_add_f32_e32 v227, 1.0, v227
	v_mfma_f32_16x16x32_f16 v[214:217], v[42:45], v[166:169], v[214:217]
	v_fma_f32 v230, v228, s41, s41
	v_rcp_f32_e32 v227, v227
	v_mfma_f32_16x16x32_f16 v[214:217], v[46:49], v[170:173], v[214:217]
	v_fma_f32 v230, v226, v230, v230
	v_rcp_f32_e32 v230, v230
	v_mfma_f32_16x16x32_f16 v[218:221], v[18:21], v[158:161], v[218:221]
	v_fma_f32 v226, -v228, v230, v230
	v_fma_f32 v200, v200, v227, v226
	v_mfma_f32_16x16x32_f16 v[218:221], v[14:17], v[162:165], v[218:221]
	v_exp_f32_e32 v226, v200
	s_nop 0
	v_add_f32_e32 v227, 1.0, v226
	v_mfma_f32_16x16x32_f16 v[218:221], v[10:13], v[166:169], v[218:221]
	v_fma_f32 v227, v229, v227, v227
	v_rcp_f32_e32 v227, v227
	v_mfma_f32_16x16x32_f16 v[218:221], v[26:29], v[170:173], v[218:221]
	v_fma_f32 v226, -v226, v227, v227
	v_exp_f32_e32 v231, v214
	v_mfma_f32_16x16x32_f16 v[222:225], v[2:5], v[158:161], v[222:225]
	v_exp_f32_e32 v232, v215
	v_min_f32_e32 v233, s42, v216
	v_mfma_f32_16x16x32_f16 v[222:225], v[6:9], v[162:165], v[222:225]
	v_exp_f32_e32 v234, v217
	v_exp_f32_e32 v233, v233
	v_mfma_f32_16x16x32_f16 v[222:225], v[22:25], v[166:169], v[222:225]
	v_exp_f32_e32 v236, v218
	v_add_f32_e32 v232, 1.0, v232
	v_mfma_f32_16x16x32_f16 v[222:225], v[30:33], v[170:173], v[222:225]
	v_fma_f32 v235, v233, s41, s41
	v_exp_f32_e32 v227, v219
	v_rcp_f32_e32 v232, v232
	v_fma_f32 v235, v231, v235, v235
	v_min_f32_e32 v228, s42, v220
	v_rcp_f32_e32 v235, v235
	s_nop 0
	v_fma_f32 v231, -v233, v235, v235
	v_exp_f32_e32 v229, v221
	v_fma_f32 v201, v201, v232, v231
	v_exp_f32_e32 v231, v201
	v_exp_f32_e32 v228, v228
	v_add_f32_e32 v232, 1.0, v231
	v_fma_f32 v232, v234, v232, v232
	v_add_f32_e32 v227, 1.0, v227
	v_rcp_f32_e32 v232, v232
	v_mfma_f32_16x16x32_f16 v[146:149], v[122:125], v[158:161], v[146:149]
	v_fma_f32 v231, -v231, v232, v232
	v_fma_f32 v230, v228, s41, s41
	v_cvt_pk_f16_f32 v246, v226, v231
	v_mfma_f32_16x16x32_f16 v[146:149], v[126:129], v[162:165], v[146:149]
	v_exp_f32_e32 v231, v222
	v_rcp_f32_e32 v227, v227
	v_exp_f32_e32 v232, v223
	buffer_load_dwordx4 v[122:125], v189, s[76:79], s46 offen
	buffer_load_dwordx4 v[126:129], v208, s[76:79], s46 offen
	v_min_f32_e32 v233, s42, v224
	v_fma_f32 v230, v236, v230, v230
	v_exp_f32_e32 v234, v225
	s_waitcnt lgkmcnt(0)
	v_mfma_f32_16x16x32_f16 v[210:213], v[70:73], v[150:153], v[98:101]
	v_exp_f32_e32 v233, v233
	v_rcp_f32_e32 v230, v230
	v_add_f32_e32 v232, 1.0, v232
	v_mfma_f32_16x16x32_f16 v[214:217], v[74:77], v[150:153], v[102:105]
	v_fma_f32 v235, v233, s41, s41
	v_fma_f32 v236, -v228, v230, v230
	v_rcp_f32_e32 v232, v232
	v_fma_f32 v235, v231, v235, v235
	v_fma_f32 v198, v198, v227, v236
	v_rcp_f32_e32 v235, v235
	s_nop 0
	v_fma_f32 v231, -v233, v235, v235
	v_exp_f32_e32 v236, v198
	v_fma_f32 v199, v199, v232, v231
	v_exp_f32_e32 v231, v199
	v_add_f32_e32 v227, 1.0, v236
	v_add_f32_e32 v232, 1.0, v231
	v_fma_f32 v232, v234, v232, v232
	v_fma_f32 v227, v229, v227, v227
	v_rcp_f32_e32 v232, v232
	s_nop 0
	v_fma_f32 v231, -v231, v232, v232
	v_rcp_f32_e32 v227, v227
	s_nop 0
	v_fma_f32 v236, -v236, v227, v227
	v_cvt_pk_f16_f32 v247, v236, v231
	ds_write_b64 v250, v[246:247] offset:12288
	v_mfma_f32_16x16x32_f16 v[210:213], v[66:69], v[154:157], v[210:213]
	v_mfma_f32_16x16x32_f16 v[214:217], v[78:81], v[154:157], v[214:217]
	buffer_load_dwordx2 v[192:193], v209, s[56:59], s45 offen
	s_waitcnt lgkmcnt(0)
	s_barrier
	ds_read_b128 v[158:161], v248 offset:4096
	ds_read_b128 v[162:165], v248 offset:5120
	ds_read_b128 v[166:169], v249 offset:6144
	ds_read_b128 v[170:173], v249 offset:7168
	v_mfma_f32_16x16x32_f16 v[218:221], v[82:85], v[150:153], v[106:109]
	v_mfma_f32_16x16x32_f16 v[222:225], v[90:93], v[150:153], v[110:113]
	v_mfma_f32_16x16x32_f16 v[218:221], v[86:89], v[154:157], v[218:221]
	v_mfma_f32_16x16x32_f16 v[222:225], v[94:97], v[154:157], v[222:225]
	s_waitcnt lgkmcnt(2)
	v_mfma_f32_16x16x32_f16 v[210:213], v[54:57], v[158:161], v[210:213]
	v_mfma_f32_16x16x32_f16 v[210:213], v[58:61], v[162:165], v[210:213]
	s_waitcnt lgkmcnt(0)
	v_mfma_f32_16x16x32_f16 v[210:213], v[62:65], v[166:169], v[210:213]
	v_mfma_f32_16x16x32_f16 v[210:213], v[50:53], v[170:173], v[210:213]
	s_waitcnt vmcnt(9)
	v_cvt_pk_f16_f32 v251, v190, v191
	ds_write_b32 v1, v251 offset:2048
	ds_read_b128 v[150:153], v186 offset:0
	ds_read_b128 v[154:157], v186 offset:1024
	s_nop 2
	v_exp_f32_e32 v226, v210
	v_exp_f32_e32 v227, v211
	v_mfma_f32_16x16x32_f16 v[214:217], v[34:37], v[158:161], v[214:217]
	v_min_f32_e32 v228, s42, v212
	v_exp_f32_e32 v229, v213
	v_mfma_f32_16x16x32_f16 v[214:217], v[38:41], v[162:165], v[214:217]
	v_exp_f32_e32 v228, v228
	v_add_f32_e32 v227, 1.0, v227
	v_mfma_f32_16x16x32_f16 v[214:217], v[42:45], v[166:169], v[214:217]
	v_fma_f32 v230, v228, s41, s41
	v_rcp_f32_e32 v227, v227
	v_mfma_f32_16x16x32_f16 v[214:217], v[46:49], v[170:173], v[214:217]
	v_fma_f32 v230, v226, v230, v230
	v_rcp_f32_e32 v230, v230
	v_mfma_f32_16x16x32_f16 v[218:221], v[18:21], v[158:161], v[218:221]
	v_fma_f32 v226, -v228, v230, v230
	v_fma_f32 v200, v200, v227, v226
	v_mfma_f32_16x16x32_f16 v[218:221], v[14:17], v[162:165], v[218:221]
	v_exp_f32_e32 v226, v200
	s_nop 0
	v_add_f32_e32 v227, 1.0, v226
	v_mfma_f32_16x16x32_f16 v[218:221], v[10:13], v[166:169], v[218:221]
	v_fma_f32 v227, v229, v227, v227
	v_rcp_f32_e32 v227, v227
	v_mfma_f32_16x16x32_f16 v[218:221], v[26:29], v[170:173], v[218:221]
	v_fma_f32 v226, -v226, v227, v227
	v_exp_f32_e32 v231, v214
	v_mfma_f32_16x16x32_f16 v[222:225], v[2:5], v[158:161], v[222:225]
	v_exp_f32_e32 v232, v215
	v_min_f32_e32 v233, s42, v216
	v_mfma_f32_16x16x32_f16 v[222:225], v[6:9], v[162:165], v[222:225]
	v_exp_f32_e32 v234, v217
	v_exp_f32_e32 v233, v233
	v_mfma_f32_16x16x32_f16 v[222:225], v[22:25], v[166:169], v[222:225]
	v_exp_f32_e32 v236, v218
	v_add_f32_e32 v232, 1.0, v232
	v_mfma_f32_16x16x32_f16 v[222:225], v[30:33], v[170:173], v[222:225]
	v_fma_f32 v235, v233, s41, s41
	v_exp_f32_e32 v227, v219
	v_rcp_f32_e32 v232, v232
	v_fma_f32 v235, v231, v235, v235
	v_min_f32_e32 v228, s42, v220
	v_rcp_f32_e32 v235, v235
	s_nop 0
	v_fma_f32 v231, -v233, v235, v235
	v_exp_f32_e32 v229, v221
	v_fma_f32 v201, v201, v232, v231
	v_exp_f32_e32 v231, v201
	v_exp_f32_e32 v228, v228
	v_add_f32_e32 v232, 1.0, v231
	v_fma_f32 v232, v234, v232, v232
	v_add_f32_e32 v227, 1.0, v227
	v_rcp_f32_e32 v232, v232
	v_mfma_f32_16x16x32_f16 v[146:149], v[114:117], v[158:161], v[146:149]
	v_fma_f32 v231, -v231, v232, v232
	v_fma_f32 v230, v228, s41, s41
	v_cvt_pk_f16_f32 v246, v226, v231
	v_mfma_f32_16x16x32_f16 v[146:149], v[118:121], v[162:165], v[146:149]
	v_exp_f32_e32 v231, v222
	v_rcp_f32_e32 v227, v227
	v_exp_f32_e32 v232, v223
	buffer_load_dwordx4 v[114:117], v189, s[80:83], s46 offen
	buffer_load_dwordx4 v[118:121], v208, s[80:83], s46 offen
	v_min_f32_e32 v233, s42, v224
	v_fma_f32 v230, v236, v230, v230
	v_exp_f32_e32 v234, v225
	s_waitcnt lgkmcnt(0)
	v_mfma_f32_16x16x32_f16 v[210:213], v[70:73], v[150:153], v[98:101]
	v_exp_f32_e32 v233, v233
	v_rcp_f32_e32 v230, v230
	v_add_f32_e32 v232, 1.0, v232
	v_mfma_f32_16x16x32_f16 v[214:217], v[74:77], v[150:153], v[102:105]
	v_fma_f32 v235, v233, s41, s41
	v_fma_f32 v236, -v228, v230, v230
	v_rcp_f32_e32 v232, v232
	v_fma_f32 v235, v231, v235, v235
	v_fma_f32 v198, v198, v227, v236
	v_rcp_f32_e32 v235, v235
	s_nop 0
	v_fma_f32 v231, -v233, v235, v235
	v_exp_f32_e32 v236, v198
	v_fma_f32 v199, v199, v232, v231
	v_exp_f32_e32 v231, v199
	v_add_f32_e32 v227, 1.0, v236
	v_add_f32_e32 v232, 1.0, v231
	v_fma_f32 v232, v234, v232, v232
	v_fma_f32 v227, v229, v227, v227
	v_rcp_f32_e32 v232, v232
	s_nop 0
	v_fma_f32 v231, -v231, v232, v232
	v_rcp_f32_e32 v227, v227
	s_nop 0
	v_fma_f32 v236, -v236, v227, v227
	v_cvt_pk_f16_f32 v247, v236, v231
	ds_write_b64 v250, v[246:247] offset:16384
	v_mfma_f32_16x16x32_f16 v[210:213], v[66:69], v[154:157], v[210:213]
	v_mfma_f32_16x16x32_f16 v[214:217], v[78:81], v[154:157], v[214:217]
	buffer_load_dwordx2 v[190:191], v209, s[60:63], s45 offen
	s_add_i32 s45, s45, 0x400000
	s_add_i32 s46, s46, 0x10000
	s_waitcnt lgkmcnt(0)
	s_barrier
	ds_read_b128 v[158:161], v248 offset:8192
	ds_read_b128 v[162:165], v248 offset:9216
	ds_read_b128 v[166:169], v249 offset:10240
	ds_read_b128 v[170:173], v249 offset:11264
	v_mfma_f32_16x16x32_f16 v[218:221], v[82:85], v[150:153], v[106:109]
	v_mfma_f32_16x16x32_f16 v[222:225], v[90:93], v[150:153], v[110:113]
	v_mfma_f32_16x16x32_f16 v[218:221], v[86:89], v[154:157], v[218:221]
	v_mfma_f32_16x16x32_f16 v[222:225], v[94:97], v[154:157], v[222:225]
	s_waitcnt lgkmcnt(2)
	v_mfma_f32_16x16x32_f16 v[210:213], v[54:57], v[158:161], v[210:213]
	v_mfma_f32_16x16x32_f16 v[210:213], v[58:61], v[162:165], v[210:213]
	s_waitcnt lgkmcnt(0)
	v_mfma_f32_16x16x32_f16 v[210:213], v[62:65], v[166:169], v[210:213]
	v_mfma_f32_16x16x32_f16 v[210:213], v[50:53], v[170:173], v[210:213]
	s_waitcnt vmcnt(9)
	v_cvt_pk_f16_f32 v251, v196, v197
	ds_write_b32 v1, v251 offset:4096
	ds_read_b128 v[150:153], v186 offset:2048
	ds_read_b128 v[154:157], v186 offset:3072
	s_nop 2
	v_exp_f32_e32 v226, v210
	v_exp_f32_e32 v227, v211
	v_mfma_f32_16x16x32_f16 v[214:217], v[34:37], v[158:161], v[214:217]
	v_min_f32_e32 v228, s42, v212
	v_exp_f32_e32 v229, v213
	v_mfma_f32_16x16x32_f16 v[214:217], v[38:41], v[162:165], v[214:217]
	v_exp_f32_e32 v228, v228
	v_add_f32_e32 v227, 1.0, v227
	v_mfma_f32_16x16x32_f16 v[214:217], v[42:45], v[166:169], v[214:217]
	v_fma_f32 v230, v228, s41, s41
	v_rcp_f32_e32 v227, v227
	v_mfma_f32_16x16x32_f16 v[214:217], v[46:49], v[170:173], v[214:217]
	v_fma_f32 v230, v226, v230, v230
	v_rcp_f32_e32 v230, v230
	v_mfma_f32_16x16x32_f16 v[218:221], v[18:21], v[158:161], v[218:221]
	v_fma_f32 v226, -v228, v230, v230
	v_fma_f32 v200, v200, v227, v226
	v_mfma_f32_16x16x32_f16 v[218:221], v[14:17], v[162:165], v[218:221]
	v_exp_f32_e32 v226, v200
	s_nop 0
	v_add_f32_e32 v227, 1.0, v226
	v_mfma_f32_16x16x32_f16 v[218:221], v[10:13], v[166:169], v[218:221]
	v_fma_f32 v227, v229, v227, v227
	v_rcp_f32_e32 v227, v227
	v_mfma_f32_16x16x32_f16 v[218:221], v[26:29], v[170:173], v[218:221]
	v_fma_f32 v226, -v226, v227, v227
	v_exp_f32_e32 v231, v214
	v_mfma_f32_16x16x32_f16 v[222:225], v[2:5], v[158:161], v[222:225]
	v_exp_f32_e32 v232, v215
	v_min_f32_e32 v233, s42, v216
	v_mfma_f32_16x16x32_f16 v[222:225], v[6:9], v[162:165], v[222:225]
	v_exp_f32_e32 v234, v217
	v_exp_f32_e32 v233, v233
	v_mfma_f32_16x16x32_f16 v[222:225], v[22:25], v[166:169], v[222:225]
	v_exp_f32_e32 v236, v218
	v_add_f32_e32 v232, 1.0, v232
	v_mfma_f32_16x16x32_f16 v[222:225], v[30:33], v[170:173], v[222:225]
	v_fma_f32 v235, v233, s41, s41
	v_exp_f32_e32 v227, v219
	v_rcp_f32_e32 v232, v232
	v_fma_f32 v235, v231, v235, v235
	v_min_f32_e32 v228, s42, v220
	v_rcp_f32_e32 v235, v235
	s_nop 0
	v_fma_f32 v231, -v233, v235, v235
	v_exp_f32_e32 v229, v221
	v_fma_f32 v201, v201, v232, v231
	v_exp_f32_e32 v231, v201
	v_exp_f32_e32 v228, v228
	v_add_f32_e32 v232, 1.0, v231
	v_fma_f32 v232, v234, v232, v232
	v_add_f32_e32 v227, 1.0, v227
	v_rcp_f32_e32 v232, v232
	v_mfma_f32_16x16x32_f16 v[146:149], v[138:141], v[158:161], v[146:149]
	v_fma_f32 v231, -v231, v232, v232
	v_fma_f32 v230, v228, s41, s41
	v_cvt_pk_f16_f32 v246, v226, v231
	v_mfma_f32_16x16x32_f16 v[146:149], v[142:145], v[162:165], v[146:149]
	v_exp_f32_e32 v231, v222
	v_rcp_f32_e32 v227, v227
	v_exp_f32_e32 v232, v223
	buffer_load_dwordx4 v[138:141], v189, s[68:71], s46 offen
	buffer_load_dwordx4 v[142:145], v208, s[68:71], s46 offen
	v_min_f32_e32 v233, s42, v224
	v_fma_f32 v230, v236, v230, v230
	v_exp_f32_e32 v234, v225
	s_waitcnt lgkmcnt(0)
	v_mfma_f32_16x16x32_f16 v[210:213], v[70:73], v[150:153], v[98:101]
	v_exp_f32_e32 v233, v233
	v_rcp_f32_e32 v230, v230
	v_add_f32_e32 v232, 1.0, v232
	v_mfma_f32_16x16x32_f16 v[214:217], v[74:77], v[150:153], v[102:105]
	v_fma_f32 v235, v233, s41, s41
	v_fma_f32 v236, -v228, v230, v230
	v_rcp_f32_e32 v232, v232
	v_fma_f32 v235, v231, v235, v235
	v_fma_f32 v198, v198, v227, v236
	v_rcp_f32_e32 v235, v235
	s_nop 0
	v_fma_f32 v231, -v233, v235, v235
	v_exp_f32_e32 v236, v198
	v_fma_f32 v199, v199, v232, v231
	v_exp_f32_e32 v231, v199
	v_add_f32_e32 v227, 1.0, v236
	v_add_f32_e32 v232, 1.0, v231
	v_fma_f32 v232, v234, v232, v232
	v_fma_f32 v227, v229, v227, v227
	v_rcp_f32_e32 v232, v232
	s_nop 0
	v_fma_f32 v231, -v231, v232, v232
	v_rcp_f32_e32 v227, v227
	s_nop 0
	v_fma_f32 v236, -v236, v227, v227
	v_cvt_pk_f16_f32 v247, v236, v231
	ds_write_b64 v250, v[246:247] offset:20480
	v_mfma_f32_16x16x32_f16 v[210:213], v[66:69], v[154:157], v[210:213]
	v_mfma_f32_16x16x32_f16 v[214:217], v[78:81], v[154:157], v[214:217]
	buffer_load_dwordx2 v[196:197], v209, s[48:51], s45 offen
	s_waitcnt lgkmcnt(0)
	s_barrier
	ds_read_b128 v[158:161], v248 offset:12288
	ds_read_b128 v[162:165], v248 offset:13312
	ds_read_b128 v[166:169], v249 offset:14336
	ds_read_b128 v[170:173], v249 offset:15360
	v_mfma_f32_16x16x32_f16 v[218:221], v[82:85], v[150:153], v[106:109]
	v_mfma_f32_16x16x32_f16 v[222:225], v[90:93], v[150:153], v[110:113]
	v_mfma_f32_16x16x32_f16 v[218:221], v[86:89], v[154:157], v[218:221]
	v_mfma_f32_16x16x32_f16 v[222:225], v[94:97], v[154:157], v[222:225]
	s_waitcnt lgkmcnt(2)
	v_mfma_f32_16x16x32_f16 v[210:213], v[54:57], v[158:161], v[210:213]
	v_mfma_f32_16x16x32_f16 v[210:213], v[58:61], v[162:165], v[210:213]
	s_waitcnt lgkmcnt(0)
	v_mfma_f32_16x16x32_f16 v[210:213], v[62:65], v[166:169], v[210:213]
	v_mfma_f32_16x16x32_f16 v[210:213], v[50:53], v[170:173], v[210:213]
	s_waitcnt vmcnt(9)
	v_cvt_pk_f16_f32 v251, v194, v195
	ds_write_b32 v1, v251 offset:6144
	ds_read_b128 v[150:153], v186 offset:4096
	ds_read_b128 v[154:157], v186 offset:5120
	s_nop 2
	v_exp_f32_e32 v226, v210
	v_exp_f32_e32 v227, v211
	v_mfma_f32_16x16x32_f16 v[214:217], v[34:37], v[158:161], v[214:217]
	v_min_f32_e32 v228, s42, v212
	v_exp_f32_e32 v229, v213
	v_mfma_f32_16x16x32_f16 v[214:217], v[38:41], v[162:165], v[214:217]
	v_exp_f32_e32 v228, v228
	v_add_f32_e32 v227, 1.0, v227
	v_mfma_f32_16x16x32_f16 v[214:217], v[42:45], v[166:169], v[214:217]
	v_fma_f32 v230, v228, s41, s41
	v_rcp_f32_e32 v227, v227
	v_mfma_f32_16x16x32_f16 v[214:217], v[46:49], v[170:173], v[214:217]
	v_fma_f32 v230, v226, v230, v230
	v_rcp_f32_e32 v230, v230
	v_mfma_f32_16x16x32_f16 v[218:221], v[18:21], v[158:161], v[218:221]
	v_fma_f32 v226, -v228, v230, v230
	v_fma_f32 v200, v200, v227, v226
	v_mfma_f32_16x16x32_f16 v[218:221], v[14:17], v[162:165], v[218:221]
	v_exp_f32_e32 v226, v200
	s_nop 0
	v_add_f32_e32 v227, 1.0, v226
	v_mfma_f32_16x16x32_f16 v[218:221], v[10:13], v[166:169], v[218:221]
	v_fma_f32 v227, v229, v227, v227
	v_rcp_f32_e32 v227, v227
	v_mfma_f32_16x16x32_f16 v[218:221], v[26:29], v[170:173], v[218:221]
	v_fma_f32 v226, -v226, v227, v227
	v_exp_f32_e32 v231, v214
	v_mfma_f32_16x16x32_f16 v[222:225], v[2:5], v[158:161], v[222:225]
	v_exp_f32_e32 v232, v215
	v_min_f32_e32 v233, s42, v216
	v_mfma_f32_16x16x32_f16 v[222:225], v[6:9], v[162:165], v[222:225]
	v_exp_f32_e32 v234, v217
	v_exp_f32_e32 v233, v233
	v_mfma_f32_16x16x32_f16 v[222:225], v[22:25], v[166:169], v[222:225]
	v_exp_f32_e32 v236, v218
	v_add_f32_e32 v232, 1.0, v232
	v_mfma_f32_16x16x32_f16 v[222:225], v[30:33], v[170:173], v[222:225]
	v_fma_f32 v235, v233, s41, s41
	v_exp_f32_e32 v227, v219
	v_rcp_f32_e32 v232, v232
	v_fma_f32 v235, v231, v235, v235
	v_min_f32_e32 v228, s42, v220
	v_rcp_f32_e32 v235, v235
	s_nop 0
	v_fma_f32 v231, -v233, v235, v235
	v_exp_f32_e32 v229, v221
	v_fma_f32 v201, v201, v232, v231
	v_exp_f32_e32 v231, v201
	v_exp_f32_e32 v228, v228
	v_add_f32_e32 v232, 1.0, v231
	v_fma_f32 v232, v234, v232, v232
	v_add_f32_e32 v227, 1.0, v227
	v_rcp_f32_e32 v232, v232
	v_mfma_f32_16x16x32_f16 v[146:149], v[130:133], v[158:161], v[146:149]
	v_fma_f32 v231, -v231, v232, v232
	v_fma_f32 v230, v228, s41, s41
	v_cvt_pk_f16_f32 v246, v226, v231
	v_mfma_f32_16x16x32_f16 v[146:149], v[134:137], v[162:165], v[146:149]
	v_exp_f32_e32 v231, v222
	v_rcp_f32_e32 v227, v227
	v_exp_f32_e32 v232, v223
	buffer_load_dwordx4 v[130:133], v189, s[72:75], s46 offen
	buffer_load_dwordx4 v[134:137], v208, s[72:75], s46 offen
	v_min_f32_e32 v233, s42, v224
	v_fma_f32 v230, v236, v230, v230
	v_exp_f32_e32 v234, v225
	s_waitcnt lgkmcnt(0)
	v_mfma_f32_16x16x32_f16 v[210:213], v[70:73], v[150:153], v[98:101]
	v_exp_f32_e32 v233, v233
	v_rcp_f32_e32 v230, v230
	v_add_f32_e32 v232, 1.0, v232
	v_mfma_f32_16x16x32_f16 v[214:217], v[74:77], v[150:153], v[102:105]
	v_fma_f32 v235, v233, s41, s41
	v_fma_f32 v236, -v228, v230, v230
	v_rcp_f32_e32 v232, v232
	v_fma_f32 v235, v231, v235, v235
	v_fma_f32 v198, v198, v227, v236
	v_rcp_f32_e32 v235, v235
	s_nop 0
	v_fma_f32 v231, -v233, v235, v235
	v_exp_f32_e32 v236, v198
	v_fma_f32 v199, v199, v232, v231
	v_exp_f32_e32 v231, v199
	v_add_f32_e32 v227, 1.0, v236
	v_add_f32_e32 v232, 1.0, v231
	v_fma_f32 v232, v234, v232, v232
	v_fma_f32 v227, v229, v227, v227
	v_rcp_f32_e32 v232, v232
	s_nop 0
	v_fma_f32 v231, -v231, v232, v232
	v_rcp_f32_e32 v227, v227
	s_nop 0
	v_fma_f32 v236, -v236, v227, v227
	v_cvt_pk_f16_f32 v247, v236, v231
	ds_write_b64 v250, v[246:247] offset:24576
	v_mfma_f32_16x16x32_f16 v[210:213], v[66:69], v[154:157], v[210:213]
	v_mfma_f32_16x16x32_f16 v[214:217], v[78:81], v[154:157], v[214:217]
	buffer_load_dwordx2 v[194:195], v209, s[52:55], s45 offen
	v_add_u32_e32 v250, 0x4000, v250
	v_add_u32_e32 v248, 0x4000, v248
	v_add_u32_e32 v249, 0x4000, v249
	s_waitcnt lgkmcnt(0)
	s_barrier
	s_cmp_lt_u32 s46, 0xa0000
	s_cbranch_scc1 .Lmy_loopb
	ds_read_b128 v[158:161], v248 offset:0
	ds_read_b128 v[162:165], v248 offset:1024
	ds_read_b128 v[166:169], v249 offset:2048
	ds_read_b128 v[170:173], v249 offset:3072
	v_mfma_f32_16x16x32_f16 v[218:221], v[82:85], v[150:153], v[106:109]
	v_mfma_f32_16x16x32_f16 v[222:225], v[90:93], v[150:153], v[110:113]
	v_mfma_f32_16x16x32_f16 v[218:221], v[86:89], v[154:157], v[218:221]
	v_mfma_f32_16x16x32_f16 v[222:225], v[94:97], v[154:157], v[222:225]
	s_waitcnt lgkmcnt(2)
	v_mfma_f32_16x16x32_f16 v[210:213], v[54:57], v[158:161], v[210:213]
	v_mfma_f32_16x16x32_f16 v[210:213], v[58:61], v[162:165], v[210:213]
	s_waitcnt lgkmcnt(0)
	v_mfma_f32_16x16x32_f16 v[210:213], v[62:65], v[166:169], v[210:213]
	v_mfma_f32_16x16x32_f16 v[210:213], v[50:53], v[170:173], v[210:213]
	s_waitcnt vmcnt(9)
	v_cvt_pk_f16_f32 v251, v192, v193
	ds_write_b32 v1, v251 offset:0
	ds_read_b128 v[150:153], v186 offset:6144
	ds_read_b128 v[154:157], v186 offset:7168
	s_nop 2
	v_exp_f32_e32 v226, v210
	v_exp_f32_e32 v227, v211
	v_mfma_f32_16x16x32_f16 v[214:217], v[34:37], v[158:161], v[214:217]
	v_min_f32_e32 v228, s42, v212
	v_exp_f32_e32 v229, v213
	v_mfma_f32_16x16x32_f16 v[214:217], v[38:41], v[162:165], v[214:217]
	v_exp_f32_e32 v228, v228
	v_add_f32_e32 v227, 1.0, v227
	v_mfma_f32_16x16x32_f16 v[214:217], v[42:45], v[166:169], v[214:217]
	v_fma_f32 v230, v228, s41, s41
	v_rcp_f32_e32 v227, v227
	v_mfma_f32_16x16x32_f16 v[214:217], v[46:49], v[170:173], v[214:217]
	v_fma_f32 v230, v226, v230, v230
	v_rcp_f32_e32 v230, v230
	v_mfma_f32_16x16x32_f16 v[218:221], v[18:21], v[158:161], v[218:221]
	v_fma_f32 v226, -v228, v230, v230
	v_fma_f32 v200, v200, v227, v226
	v_mfma_f32_16x16x32_f16 v[218:221], v[14:17], v[162:165], v[218:221]
	v_min_f32_e32 v226, s42, v200
	v_exp_f32_e32 v226, v226
	v_mfma_f32_16x16x32_f16 v[218:221], v[10:13], v[166:169], v[218:221]
	v_add_f32_e32 v227, 1.0, v226
	v_fma_f32 v227, v229, v227, v227
	v_mfma_f32_16x16x32_f16 v[218:221], v[26:29], v[170:173], v[218:221]
	v_rcp_f32_e32 v227, v227
	v_exp_f32_e32 v231, v214
	v_mfma_f32_16x16x32_f16 v[222:225], v[2:5], v[158:161], v[222:225]
	v_exp_f32_e32 v232, v215
	v_fma_f32 v226, -v226, v227, v227
	v_mfma_f32_16x16x32_f16 v[222:225], v[6:9], v[162:165], v[222:225]
	v_min_f32_e32 v233, s42, v216
	v_exp_f32_e32 v234, v217
	v_mfma_f32_16x16x32_f16 v[222:225], v[22:25], v[166:169], v[222:225]
	v_exp_f32_e32 v236, v218
	v_exp_f32_e32 v233, v233
	v_mfma_f32_16x16x32_f16 v[222:225], v[30:33], v[170:173], v[222:225]
	v_add_f32_e32 v232, 1.0, v232
	v_exp_f32_e32 v227, v219
	v_fma_f32 v235, v233, s41, s41
	v_rcp_f32_e32 v232, v232
	v_min_f32_e32 v228, s42, v220
	v_fma_f32 v235, v231, v235, v235
	v_rcp_f32_e32 v235, v235
	v_exp_f32_e32 v229, v221
	v_fma_f32 v231, -v233, v235, v235
	v_fma_f32 v201, v201, v232, v231
	v_exp_f32_e32 v228, v228
	v_min_f32_e32 v231, s42, v201
	v_exp_f32_e32 v231, v231
	v_add_f32_e32 v227, 1.0, v227
	v_add_f32_e32 v232, 1.0, v231
	v_mfma_f32_16x16x32_f16 v[146:149], v[122:125], v[158:161], v[146:149]
	v_fma_f32 v232, v234, v232, v232
	v_fma_f32 v230, v228, s41, s41
	v_rcp_f32_e32 v232, v232
	v_mfma_f32_16x16x32_f16 v[146:149], v[126:129], v[162:165], v[146:149]
	v_fma_f32 v231, -v231, v232, v232
	v_rcp_f32_e32 v227, v227
	v_cvt_pk_f16_f32 v246, v226, v231
	buffer_load_dwordx4 v[122:125], v189, s[76:79], s46 offen
	buffer_load_dwordx4 v[126:129], v208, s[76:79], s46 offen
	v_exp_f32_e32 v231, v222
	v_fma_f32 v230, v236, v230, v230
	v_exp_f32_e32 v232, v223
	s_waitcnt lgkmcnt(0)
	v_mfma_f32_16x16x32_f16 v[210:213], v[70:73], v[150:153], v[98:101]
	v_min_f32_e32 v233, s42, v224
	v_rcp_f32_e32 v230, v230
	v_exp_f32_e32 v234, v225
	v_mfma_f32_16x16x32_f16 v[214:217], v[74:77], v[150:153], v[102:105]
	v_exp_f32_e32 v233, v233
	v_fma_f32 v236, -v228, v230, v230
	v_add_f32_e32 v232, 1.0, v232
	v_fma_f32 v235, v233, s41, s41
	v_fma_f32 v198, v198, v227, v236
	v_rcp_f32_e32 v232, v232
	v_fma_f32 v235, v231, v235, v235
	v_min_f32_e32 v236, s42, v198
	v_rcp_f32_e32 v235, v235
	s_nop 0
	v_fma_f32 v231, -v233, v235, v235
	v_exp_f32_e32 v236, v236
	v_fma_f32 v199, v199, v232, v231
	v_min_f32_e32 v231, s42, v199
	v_add_f32_e32 v227, 1.0, v236
	v_exp_f32_e32 v231, v231
	v_fma_f32 v227, v229, v227, v227
	v_add_f32_e32 v232, 1.0, v231
	v_rcp_f32_e32 v227, v227
	v_fma_f32 v232, v234, v232, v232
	v_fma_f32 v236, -v236, v227, v227
	v_rcp_f32_e32 v232, v232
	s_nop 0
	v_fma_f32 v231, -v231, v232, v232
	v_cvt_pk_f16_f32 v247, v236, v231
	ds_write_b64 v250, v[246:247] offset:12288
	v_mfma_f32_16x16x32_f16 v[210:213], v[66:69], v[154:157], v[210:213]
	v_mfma_f32_16x16x32_f16 v[214:217], v[78:81], v[154:157], v[214:217]
	buffer_load_dwordx2 v[192:193], v209, s[56:59], s45 offen
	s_waitcnt lgkmcnt(0)
	s_barrier
	ds_read_b128 v[158:161], v248 offset:4096
	ds_read_b128 v[162:165], v248 offset:5120
	ds_read_b128 v[166:169], v249 offset:6144
	ds_read_b128 v[170:173], v249 offset:7168
	v_mfma_f32_16x16x32_f16 v[218:221], v[82:85], v[150:153], v[106:109]
	v_mfma_f32_16x16x32_f16 v[222:225], v[90:93], v[150:153], v[110:113]
	v_mfma_f32_16x16x32_f16 v[218:221], v[86:89], v[154:157], v[218:221]
	v_mfma_f32_16x16x32_f16 v[222:225], v[94:97], v[154:157], v[222:225]
	s_waitcnt lgkmcnt(2)
	v_mfma_f32_16x16x32_f16 v[210:213], v[54:57], v[158:161], v[210:213]
	v_mfma_f32_16x16x32_f16 v[210:213], v[58:61], v[162:165], v[210:213]
	s_waitcnt lgkmcnt(0)
	v_mfma_f32_16x16x32_f16 v[210:213], v[62:65], v[166:169], v[210:213]
	v_mfma_f32_16x16x32_f16 v[210:213], v[50:53], v[170:173], v[210:213]
	s_waitcnt vmcnt(9)
	v_cvt_pk_f16_f32 v251, v190, v191
	ds_write_b32 v1, v251 offset:2048
	ds_read_b128 v[150:153], v186 offset:0
	ds_read_b128 v[154:157], v186 offset:1024
	s_nop 2
	v_exp_f32_e32 v226, v210
	v_exp_f32_e32 v227, v211
	v_mfma_f32_16x16x32_f16 v[214:217], v[34:37], v[158:161], v[214:217]
	v_min_f32_e32 v228, s42, v212
	v_exp_f32_e32 v229, v213
	v_mfma_f32_16x16x32_f16 v[214:217], v[38:41], v[162:165], v[214:217]
	v_exp_f32_e32 v228, v228
	v_add_f32_e32 v227, 1.0, v227
	v_mfma_f32_16x16x32_f16 v[214:217], v[42:45], v[166:169], v[214:217]
	v_fma_f32 v230, v228, s41, s41
	v_rcp_f32_e32 v227, v227
	v_mfma_f32_16x16x32_f16 v[214:217], v[46:49], v[170:173], v[214:217]
	v_fma_f32 v230, v226, v230, v230
	v_rcp_f32_e32 v230, v230
	v_mfma_f32_16x16x32_f16 v[218:221], v[18:21], v[158:161], v[218:221]
	v_fma_f32 v226, -v228, v230, v230
	v_fma_f32 v200, v200, v227, v226
	v_mfma_f32_16x16x32_f16 v[218:221], v[14:17], v[162:165], v[218:221]
	v_min_f32_e32 v226, s42, v200
	v_exp_f32_e32 v226, v226
	v_mfma_f32_16x16x32_f16 v[218:221], v[10:13], v[166:169], v[218:221]
	v_add_f32_e32 v227, 1.0, v226
	v_fma_f32 v227, v229, v227, v227
	v_mfma_f32_16x16x32_f16 v[218:221], v[26:29], v[170:173], v[218:221]
	v_rcp_f32_e32 v227, v227
	v_exp_f32_e32 v231, v214
	v_mfma_f32_16x16x32_f16 v[222:225], v[2:5], v[158:161], v[222:225]
	v_exp_f32_e32 v232, v215
	v_fma_f32 v226, -v226, v227, v227
	v_mfma_f32_16x16x32_f16 v[222:225], v[6:9], v[162:165], v[222:225]
	v_min_f32_e32 v233, s42, v216
	v_exp_f32_e32 v234, v217
	v_mfma_f32_16x16x32_f16 v[222:225], v[22:25], v[166:169], v[222:225]
	v_exp_f32_e32 v236, v218
	v_exp_f32_e32 v233, v233
	v_mfma_f32_16x16x32_f16 v[222:225], v[30:33], v[170:173], v[222:225]
	v_add_f32_e32 v232, 1.0, v232
	v_exp_f32_e32 v227, v219
	v_fma_f32 v235, v233, s41, s41
	v_rcp_f32_e32 v232, v232
	v_min_f32_e32 v228, s42, v220
	v_fma_f32 v235, v231, v235, v235
	v_rcp_f32_e32 v235, v235
	v_exp_f32_e32 v229, v221
	v_fma_f32 v231, -v233, v235, v235
	v_fma_f32 v201, v201, v232, v231
	v_exp_f32_e32 v228, v228
	v_min_f32_e32 v231, s42, v201
	v_exp_f32_e32 v231, v231
	v_add_f32_e32 v227, 1.0, v227
	v_add_f32_e32 v232, 1.0, v231
	v_mfma_f32_16x16x32_f16 v[146:149], v[114:117], v[158:161], v[146:149]
	v_fma_f32 v232, v234, v232, v232
	v_fma_f32 v230, v228, s41, s41
	v_rcp_f32_e32 v232, v232
	v_mfma_f32_16x16x32_f16 v[146:149], v[118:121], v[162:165], v[146:149]
	v_fma_f32 v231, -v231, v232, v232
	v_rcp_f32_e32 v227, v227
	v_cvt_pk_f16_f32 v246, v226, v231
	buffer_load_dwordx4 v[114:117], v189, s[80:83], s46 offen
	buffer_load_dwordx4 v[118:121], v208, s[80:83], s46 offen
	v_exp_f32_e32 v231, v222
	v_fma_f32 v230, v236, v230, v230
	v_exp_f32_e32 v232, v223
	s_waitcnt lgkmcnt(0)
	v_mfma_f32_16x16x32_f16 v[210:213], v[70:73], v[150:153], v[98:101]
	v_min_f32_e32 v233, s42, v224
	v_rcp_f32_e32 v230, v230
	v_exp_f32_e32 v234, v225
	v_mfma_f32_16x16x32_f16 v[214:217], v[74:77], v[150:153], v[102:105]
	v_exp_f32_e32 v233, v233
	v_fma_f32 v236, -v228, v230, v230
	v_add_f32_e32 v232, 1.0, v232
	v_fma_f32 v235, v233, s41, s41
	v_fma_f32 v198, v198, v227, v236
	v_rcp_f32_e32 v232, v232
	v_fma_f32 v235, v231, v235, v235
	v_min_f32_e32 v236, s42, v198
	v_rcp_f32_e32 v235, v235
	s_nop 0
	v_fma_f32 v231, -v233, v235, v235
	v_exp_f32_e32 v236, v236
	v_fma_f32 v199, v199, v232, v231
	v_min_f32_e32 v231, s42, v199
	v_add_f32_e32 v227, 1.0, v236
	v_exp_f32_e32 v231, v231
	v_fma_f32 v227, v229, v227, v227
	v_add_f32_e32 v232, 1.0, v231
	v_rcp_f32_e32 v227, v227
	v_fma_f32 v232, v234, v232, v232
	v_fma_f32 v236, -v236, v227, v227
	v_rcp_f32_e32 v232, v232
	s_nop 0
	v_fma_f32 v231, -v231, v232, v232
	v_cvt_pk_f16_f32 v247, v236, v231
	ds_write_b64 v250, v[246:247] offset:16384
	v_mfma_f32_16x16x32_f16 v[210:213], v[66:69], v[154:157], v[210:213]
	v_mfma_f32_16x16x32_f16 v[214:217], v[78:81], v[154:157], v[214:217]
	buffer_load_dwordx2 v[190:191], v209, s[60:63], s45 offen
	s_add_i32 s45, s45, 0x400000
	s_add_i32 s46, s46, 0x10000
	s_waitcnt lgkmcnt(0)
	s_barrier
	ds_read_b128 v[158:161], v248 offset:8192
	ds_read_b128 v[162:165], v248 offset:9216
	ds_read_b128 v[166:169], v249 offset:10240
	ds_read_b128 v[170:173], v249 offset:11264
	v_mfma_f32_16x16x32_f16 v[218:221], v[82:85], v[150:153], v[106:109]
	v_mfma_f32_16x16x32_f16 v[222:225], v[90:93], v[150:153], v[110:113]
	v_mfma_f32_16x16x32_f16 v[218:221], v[86:89], v[154:157], v[218:221]
	v_mfma_f32_16x16x32_f16 v[222:225], v[94:97], v[154:157], v[222:225]
	s_waitcnt lgkmcnt(2)
	v_mfma_f32_16x16x32_f16 v[210:213], v[54:57], v[158:161], v[210:213]
	v_mfma_f32_16x16x32_f16 v[210:213], v[58:61], v[162:165], v[210:213]
	s_waitcnt lgkmcnt(0)
	v_mfma_f32_16x16x32_f16 v[210:213], v[62:65], v[166:169], v[210:213]
	v_mfma_f32_16x16x32_f16 v[210:213], v[50:53], v[170:173], v[210:213]
	s_waitcnt vmcnt(9)
	v_cvt_pk_f16_f32 v251, v196, v197
	ds_write_b32 v1, v251 offset:4096
	ds_read_b128 v[150:153], v186 offset:2048
	ds_read_b128 v[154:157], v186 offset:3072
	s_nop 2
	v_exp_f32_e32 v226, v210
	v_exp_f32_e32 v227, v211
	v_mfma_f32_16x16x32_f16 v[214:217], v[34:37], v[158:161], v[214:217]
	v_min_f32_e32 v228, s42, v212
	v_exp_f32_e32 v229, v213
	v_mfma_f32_16x16x32_f16 v[214:217], v[38:41], v[162:165], v[214:217]
	v_exp_f32_e32 v228, v228
	v_add_f32_e32 v227, 1.0, v227
	v_mfma_f32_16x16x32_f16 v[214:217], v[42:45], v[166:169], v[214:217]
	v_fma_f32 v230, v228, s41, s41
	v_rcp_f32_e32 v227, v227
	v_mfma_f32_16x16x32_f16 v[214:217], v[46:49], v[170:173], v[214:217]
	v_fma_f32 v230, v226, v230, v230
	v_rcp_f32_e32 v230, v230
	v_mfma_f32_16x16x32_f16 v[218:221], v[18:21], v[158:161], v[218:221]
	v_fma_f32 v226, -v228, v230, v230
	v_fma_f32 v200, v200, v227, v226
	v_mfma_f32_16x16x32_f16 v[218:221], v[14:17], v[162:165], v[218:221]
	v_min_f32_e32 v226, s42, v200
	v_exp_f32_e32 v226, v226
	v_mfma_f32_16x16x32_f16 v[218:221], v[10:13], v[166:169], v[218:221]
	v_add_f32_e32 v227, 1.0, v226
	v_fma_f32 v227, v229, v227, v227
	v_mfma_f32_16x16x32_f16 v[218:221], v[26:29], v[170:173], v[218:221]
	v_rcp_f32_e32 v227, v227
	v_exp_f32_e32 v231, v214
	v_mfma_f32_16x16x32_f16 v[222:225], v[2:5], v[158:161], v[222:225]
	v_exp_f32_e32 v232, v215
	v_fma_f32 v226, -v226, v227, v227
	v_mfma_f32_16x16x32_f16 v[222:225], v[6:9], v[162:165], v[222:225]
	v_min_f32_e32 v233, s42, v216
	v_exp_f32_e32 v234, v217
	v_mfma_f32_16x16x32_f16 v[222:225], v[22:25], v[166:169], v[222:225]
	v_exp_f32_e32 v236, v218
	v_exp_f32_e32 v233, v233
	v_mfma_f32_16x16x32_f16 v[222:225], v[30:33], v[170:173], v[222:225]
	v_add_f32_e32 v232, 1.0, v232
	v_exp_f32_e32 v227, v219
	v_fma_f32 v235, v233, s41, s41
	v_rcp_f32_e32 v232, v232
	v_min_f32_e32 v228, s42, v220
	v_fma_f32 v235, v231, v235, v235
	v_rcp_f32_e32 v235, v235
	v_exp_f32_e32 v229, v221
	v_fma_f32 v231, -v233, v235, v235
	v_fma_f32 v201, v201, v232, v231
	v_exp_f32_e32 v228, v228
	v_min_f32_e32 v231, s42, v201
	v_exp_f32_e32 v231, v231
	v_add_f32_e32 v227, 1.0, v227
	v_add_f32_e32 v232, 1.0, v231
	v_mfma_f32_16x16x32_f16 v[146:149], v[138:141], v[158:161], v[146:149]
	v_fma_f32 v232, v234, v232, v232
	v_fma_f32 v230, v228, s41, s41
	v_rcp_f32_e32 v232, v232
	v_mfma_f32_16x16x32_f16 v[146:149], v[142:145], v[162:165], v[146:149]
	v_fma_f32 v231, -v231, v232, v232
	v_rcp_f32_e32 v227, v227
	v_cvt_pk_f16_f32 v246, v226, v231
	buffer_load_dwordx4 v[138:141], v189, s[68:71], s46 offen
	buffer_load_dwordx4 v[142:145], v208, s[68:71], s46 offen
	v_exp_f32_e32 v231, v222
	v_fma_f32 v230, v236, v230, v230
	v_exp_f32_e32 v232, v223
	s_waitcnt lgkmcnt(0)
	v_mfma_f32_16x16x32_f16 v[210:213], v[70:73], v[150:153], v[98:101]
	v_min_f32_e32 v233, s42, v224
	v_rcp_f32_e32 v230, v230
	v_exp_f32_e32 v234, v225
	v_mfma_f32_16x16x32_f16 v[214:217], v[74:77], v[150:153], v[102:105]
	v_exp_f32_e32 v233, v233
	v_fma_f32 v236, -v228, v230, v230
	v_add_f32_e32 v232, 1.0, v232
	v_fma_f32 v235, v233, s41, s41
	v_fma_f32 v198, v198, v227, v236
	v_rcp_f32_e32 v232, v232
	v_fma_f32 v235, v231, v235, v235
	v_min_f32_e32 v236, s42, v198
	v_rcp_f32_e32 v235, v235
	s_nop 0
	v_fma_f32 v231, -v233, v235, v235
	v_exp_f32_e32 v236, v236
	v_fma_f32 v199, v199, v232, v231
	v_min_f32_e32 v231, s42, v199
	v_add_f32_e32 v227, 1.0, v236
	v_exp_f32_e32 v231, v231
	v_fma_f32 v227, v229, v227, v227
	v_add_f32_e32 v232, 1.0, v231
	v_rcp_f32_e32 v227, v227
	v_fma_f32 v232, v234, v232, v232
	v_fma_f32 v236, -v236, v227, v227
	v_rcp_f32_e32 v232, v232
	s_nop 0
	v_fma_f32 v231, -v231, v232, v232
	v_cvt_pk_f16_f32 v247, v236, v231
	ds_write_b64 v250, v[246:247] offset:20480
	v_mfma_f32_16x16x32_f16 v[210:213], v[66:69], v[154:157], v[210:213]
	v_mfma_f32_16x16x32_f16 v[214:217], v[78:81], v[154:157], v[214:217]
	s_waitcnt lgkmcnt(0)
	s_barrier
	ds_read_b128 v[158:161], v248 offset:12288
	ds_read_b128 v[162:165], v248 offset:13312
	ds_read_b128 v[166:169], v249 offset:14336
	ds_read_b128 v[170:173], v249 offset:15360
	v_mfma_f32_16x16x32_f16 v[218:221], v[82:85], v[150:153], v[106:109]
	v_mfma_f32_16x16x32_f16 v[222:225], v[90:93], v[150:153], v[110:113]
	v_mfma_f32_16x16x32_f16 v[218:221], v[86:89], v[154:157], v[218:221]
	v_mfma_f32_16x16x32_f16 v[222:225], v[94:97], v[154:157], v[222:225]
	s_waitcnt lgkmcnt(2)
	v_mfma_f32_16x16x32_f16 v[210:213], v[54:57], v[158:161], v[210:213]
	v_mfma_f32_16x16x32_f16 v[210:213], v[58:61], v[162:165], v[210:213]
	s_waitcnt lgkmcnt(0)
	v_mfma_f32_16x16x32_f16 v[210:213], v[62:65], v[166:169], v[210:213]
	v_mfma_f32_16x16x32_f16 v[210:213], v[50:53], v[170:173], v[210:213]
	s_waitcnt vmcnt(8)
	v_cvt_pk_f16_f32 v251, v194, v195
	ds_write_b32 v1, v251 offset:6144
	ds_read_b128 v[150:153], v186 offset:4096
	ds_read_b128 v[154:157], v186 offset:5120
	s_nop 2
	v_exp_f32_e32 v226, v210
	v_exp_f32_e32 v227, v211
	v_mfma_f32_16x16x32_f16 v[214:217], v[34:37], v[158:161], v[214:217]
	v_min_f32_e32 v228, s42, v212
	v_exp_f32_e32 v229, v213
	v_mfma_f32_16x16x32_f16 v[214:217], v[38:41], v[162:165], v[214:217]
	v_exp_f32_e32 v228, v228
	v_add_f32_e32 v227, 1.0, v227
	v_mfma_f32_16x16x32_f16 v[214:217], v[42:45], v[166:169], v[214:217]
	v_fma_f32 v230, v228, s41, s41
	v_rcp_f32_e32 v227, v227
	v_mfma_f32_16x16x32_f16 v[214:217], v[46:49], v[170:173], v[214:217]
	v_fma_f32 v230, v226, v230, v230
	v_rcp_f32_e32 v230, v230
	v_mfma_f32_16x16x32_f16 v[218:221], v[18:21], v[158:161], v[218:221]
	v_fma_f32 v226, -v228, v230, v230
	v_fma_f32 v200, v200, v227, v226
	v_mfma_f32_16x16x32_f16 v[218:221], v[14:17], v[162:165], v[218:221]
	v_min_f32_e32 v226, s42, v200
	v_exp_f32_e32 v226, v226
	v_mfma_f32_16x16x32_f16 v[218:221], v[10:13], v[166:169], v[218:221]
	v_add_f32_e32 v227, 1.0, v226
	v_fma_f32 v227, v229, v227, v227
	v_mfma_f32_16x16x32_f16 v[218:221], v[26:29], v[170:173], v[218:221]
	v_rcp_f32_e32 v227, v227
	v_exp_f32_e32 v231, v214
	v_mfma_f32_16x16x32_f16 v[222:225], v[2:5], v[158:161], v[222:225]
	v_exp_f32_e32 v232, v215
	v_fma_f32 v226, -v226, v227, v227
	v_mfma_f32_16x16x32_f16 v[222:225], v[6:9], v[162:165], v[222:225]
	v_min_f32_e32 v233, s42, v216
	v_exp_f32_e32 v234, v217
	v_mfma_f32_16x16x32_f16 v[222:225], v[22:25], v[166:169], v[222:225]
	v_exp_f32_e32 v236, v218
	v_exp_f32_e32 v233, v233
	v_mfma_f32_16x16x32_f16 v[222:225], v[30:33], v[170:173], v[222:225]
	v_add_f32_e32 v232, 1.0, v232
	v_exp_f32_e32 v227, v219
	v_fma_f32 v235, v233, s41, s41
	v_rcp_f32_e32 v232, v232
	v_min_f32_e32 v228, s42, v220
	v_fma_f32 v235, v231, v235, v235
	v_rcp_f32_e32 v235, v235
	v_exp_f32_e32 v229, v221
	v_fma_f32 v231, -v233, v235, v235
	v_fma_f32 v201, v201, v232, v231
	v_exp_f32_e32 v228, v228
	v_min_f32_e32 v231, s42, v201
	v_exp_f32_e32 v231, v231
	v_add_f32_e32 v227, 1.0, v227
	v_add_f32_e32 v232, 1.0, v231
	v_mfma_f32_16x16x32_f16 v[146:149], v[130:133], v[158:161], v[146:149]
	v_fma_f32 v232, v234, v232, v232
	v_fma_f32 v230, v228, s41, s41
	v_rcp_f32_e32 v232, v232
	v_mfma_f32_16x16x32_f16 v[146:149], v[134:137], v[162:165], v[146:149]
	v_fma_f32 v231, -v231, v232, v232
	v_rcp_f32_e32 v227, v227
	v_cvt_pk_f16_f32 v246, v226, v231
	buffer_load_dwordx4 v[130:133], v189, s[72:75], s46 offen
	buffer_load_dwordx4 v[134:137], v208, s[72:75], s46 offen
	v_exp_f32_e32 v231, v222
	v_fma_f32 v230, v236, v230, v230
	v_exp_f32_e32 v232, v223
	s_waitcnt lgkmcnt(0)
	v_mfma_f32_16x16x32_f16 v[210:213], v[70:73], v[150:153], v[98:101]
	v_min_f32_e32 v233, s42, v224
	v_rcp_f32_e32 v230, v230
	v_exp_f32_e32 v234, v225
	v_mfma_f32_16x16x32_f16 v[214:217], v[74:77], v[150:153], v[102:105]
	v_exp_f32_e32 v233, v233
	v_fma_f32 v236, -v228, v230, v230
	v_add_f32_e32 v232, 1.0, v232
	v_fma_f32 v235, v233, s41, s41
	v_fma_f32 v198, v198, v227, v236
	v_rcp_f32_e32 v232, v232
	v_fma_f32 v235, v231, v235, v235
	v_min_f32_e32 v236, s42, v198
	v_rcp_f32_e32 v235, v235
	s_nop 0
	v_fma_f32 v231, -v233, v235, v235
	v_exp_f32_e32 v236, v236
	v_fma_f32 v199, v199, v232, v231
	v_min_f32_e32 v231, s42, v199
	v_add_f32_e32 v227, 1.0, v236
	v_exp_f32_e32 v231, v231
	v_fma_f32 v227, v229, v227, v227
	v_add_f32_e32 v232, 1.0, v231
	v_rcp_f32_e32 v227, v227
	v_fma_f32 v232, v234, v232, v232
	v_fma_f32 v236, -v236, v227, v227
	v_rcp_f32_e32 v232, v232
	s_nop 0
	v_fma_f32 v231, -v231, v232, v232
	v_cvt_pk_f16_f32 v247, v236, v231
	ds_write_b64 v250, v[246:247] offset:24576
	v_mfma_f32_16x16x32_f16 v[210:213], v[66:69], v[154:157], v[210:213]
	v_mfma_f32_16x16x32_f16 v[214:217], v[78:81], v[154:157], v[214:217]
	v_add_u32_e32 v250, 0x4000, v250
	v_add_u32_e32 v248, 0x4000, v248
	v_add_u32_e32 v249, 0x4000, v249
	s_waitcnt lgkmcnt(0)
	s_barrier
	ds_read_b128 v[158:161], v248 offset:0
	ds_read_b128 v[162:165], v248 offset:1024
	ds_read_b128 v[166:169], v249 offset:2048
	ds_read_b128 v[170:173], v249 offset:3072
	v_mfma_f32_16x16x32_f16 v[218:221], v[82:85], v[150:153], v[106:109]
	v_mfma_f32_16x16x32_f16 v[222:225], v[90:93], v[150:153], v[110:113]
	v_mfma_f32_16x16x32_f16 v[218:221], v[86:89], v[154:157], v[218:221]
	v_mfma_f32_16x16x32_f16 v[222:225], v[94:97], v[154:157], v[222:225]
	s_waitcnt lgkmcnt(2)
	v_mfma_f32_16x16x32_f16 v[210:213], v[54:57], v[158:161], v[210:213]
	v_mfma_f32_16x16x32_f16 v[210:213], v[58:61], v[162:165], v[210:213]
	s_waitcnt lgkmcnt(0)
	v_mfma_f32_16x16x32_f16 v[210:213], v[62:65], v[166:169], v[210:213]
	v_mfma_f32_16x16x32_f16 v[210:213], v[50:53], v[170:173], v[210:213]
	s_waitcnt vmcnt(7)
	v_cvt_pk_f16_f32 v251, v192, v193
	ds_write_b32 v1, v251 offset:0
	ds_read_b128 v[150:153], v186 offset:6144
	ds_read_b128 v[154:157], v186 offset:7168
	s_nop 2
	v_exp_f32_e32 v226, v210
	v_exp_f32_e32 v227, v211
	v_mfma_f32_16x16x32_f16 v[214:217], v[34:37], v[158:161], v[214:217]
	v_min_f32_e32 v228, s42, v212
	v_exp_f32_e32 v229, v213
	v_mfma_f32_16x16x32_f16 v[214:217], v[38:41], v[162:165], v[214:217]
	v_exp_f32_e32 v228, v228
	v_add_f32_e32 v227, 1.0, v227
	v_mfma_f32_16x16x32_f16 v[214:217], v[42:45], v[166:169], v[214:217]
	v_fma_f32 v230, v228, s41, s41
	v_rcp_f32_e32 v227, v227
	v_mfma_f32_16x16x32_f16 v[214:217], v[46:49], v[170:173], v[214:217]
	v_fma_f32 v230, v226, v230, v230
	v_rcp_f32_e32 v230, v230
	v_mfma_f32_16x16x32_f16 v[218:221], v[18:21], v[158:161], v[218:221]
	v_fma_f32 v226, -v228, v230, v230
	v_fma_f32 v200, v200, v227, v226
	v_mfma_f32_16x16x32_f16 v[218:221], v[14:17], v[162:165], v[218:221]
	v_min_f32_e32 v226, s42, v200
	v_exp_f32_e32 v226, v226
	v_mfma_f32_16x16x32_f16 v[218:221], v[10:13], v[166:169], v[218:221]
	v_add_f32_e32 v227, 1.0, v226
	v_fma_f32 v227, v229, v227, v227
	v_mfma_f32_16x16x32_f16 v[218:221], v[26:29], v[170:173], v[218:221]
	v_rcp_f32_e32 v227, v227
	v_exp_f32_e32 v231, v214
	v_mfma_f32_16x16x32_f16 v[222:225], v[2:5], v[158:161], v[222:225]
	v_exp_f32_e32 v232, v215
	v_fma_f32 v226, -v226, v227, v227
	v_mfma_f32_16x16x32_f16 v[222:225], v[6:9], v[162:165], v[222:225]
	v_min_f32_e32 v233, s42, v216
	v_exp_f32_e32 v234, v217
	v_mfma_f32_16x16x32_f16 v[222:225], v[22:25], v[166:169], v[222:225]
	v_exp_f32_e32 v236, v218
	v_exp_f32_e32 v233, v233
	v_mfma_f32_16x16x32_f16 v[222:225], v[30:33], v[170:173], v[222:225]
	v_add_f32_e32 v232, 1.0, v232
	v_exp_f32_e32 v227, v219
	v_fma_f32 v235, v233, s41, s41
	v_rcp_f32_e32 v232, v232
	v_min_f32_e32 v228, s42, v220
	v_fma_f32 v235, v231, v235, v235
	v_rcp_f32_e32 v235, v235
	v_exp_f32_e32 v229, v221
	v_fma_f32 v231, -v233, v235, v235
	v_fma_f32 v201, v201, v232, v231
	v_exp_f32_e32 v228, v228
	v_min_f32_e32 v231, s42, v201
	v_exp_f32_e32 v231, v231
	v_add_f32_e32 v227, 1.0, v227
	v_add_f32_e32 v232, 1.0, v231
	v_mfma_f32_16x16x32_f16 v[146:149], v[122:125], v[158:161], v[146:149]
	v_fma_f32 v232, v234, v232, v232
	v_fma_f32 v230, v228, s41, s41
	v_rcp_f32_e32 v232, v232
	v_mfma_f32_16x16x32_f16 v[146:149], v[126:129], v[162:165], v[146:149]
	v_fma_f32 v231, -v231, v232, v232
	v_rcp_f32_e32 v227, v227
	v_cvt_pk_f16_f32 v246, v226, v231
	buffer_load_dwordx4 v[122:125], v189, s[76:79], s46 offen
	buffer_load_dwordx4 v[126:129], v208, s[76:79], s46 offen
	v_exp_f32_e32 v231, v222
	v_fma_f32 v230, v236, v230, v230
	v_exp_f32_e32 v232, v223
	s_waitcnt lgkmcnt(0)
	v_mfma_f32_16x16x32_f16 v[210:213], v[70:73], v[150:153], v[98:101]
	v_min_f32_e32 v233, s42, v224
	v_rcp_f32_e32 v230, v230
	v_exp_f32_e32 v234, v225
	v_mfma_f32_16x16x32_f16 v[214:217], v[74:77], v[150:153], v[102:105]
	v_exp_f32_e32 v233, v233
	v_fma_f32 v236, -v228, v230, v230
	v_add_f32_e32 v232, 1.0, v232
	v_fma_f32 v235, v233, s41, s41
	v_fma_f32 v198, v198, v227, v236
	v_rcp_f32_e32 v232, v232
	v_fma_f32 v235, v231, v235, v235
	v_min_f32_e32 v236, s42, v198
	v_rcp_f32_e32 v235, v235
	s_nop 0
	v_fma_f32 v231, -v233, v235, v235
	v_exp_f32_e32 v236, v236
	v_fma_f32 v199, v199, v232, v231
	v_min_f32_e32 v231, s42, v199
	v_add_f32_e32 v227, 1.0, v236
	v_exp_f32_e32 v231, v231
	v_fma_f32 v227, v229, v227, v227
	v_add_f32_e32 v232, 1.0, v231
	v_rcp_f32_e32 v227, v227
	v_fma_f32 v232, v234, v232, v232
	v_fma_f32 v236, -v236, v227, v227
	v_rcp_f32_e32 v232, v232
	s_nop 0
	v_fma_f32 v231, -v231, v232, v232
	v_cvt_pk_f16_f32 v247, v236, v231
	ds_write_b64 v250, v[246:247] offset:12288
	v_mfma_f32_16x16x32_f16 v[210:213], v[66:69], v[154:157], v[210:213]
	v_mfma_f32_16x16x32_f16 v[214:217], v[78:81], v[154:157], v[214:217]
	s_waitcnt lgkmcnt(0)
	s_barrier
	ds_read_b128 v[158:161], v248 offset:4096
	ds_read_b128 v[162:165], v248 offset:5120
	ds_read_b128 v[166:169], v249 offset:6144
	ds_read_b128 v[170:173], v249 offset:7168
	v_mfma_f32_16x16x32_f16 v[218:221], v[82:85], v[150:153], v[106:109]
	v_mfma_f32_16x16x32_f16 v[222:225], v[90:93], v[150:153], v[110:113]
	v_mfma_f32_16x16x32_f16 v[218:221], v[86:89], v[154:157], v[218:221]
	v_mfma_f32_16x16x32_f16 v[222:225], v[94:97], v[154:157], v[222:225]
	s_waitcnt lgkmcnt(2)
	v_mfma_f32_16x16x32_f16 v[210:213], v[54:57], v[158:161], v[210:213]
	v_mfma_f32_16x16x32_f16 v[210:213], v[58:61], v[162:165], v[210:213]
	s_waitcnt lgkmcnt(0)
	v_mfma_f32_16x16x32_f16 v[210:213], v[62:65], v[166:169], v[210:213]
	v_mfma_f32_16x16x32_f16 v[210:213], v[50:53], v[170:173], v[210:213]
	s_waitcnt vmcnt(6)
	v_cvt_pk_f16_f32 v251, v190, v191
	ds_write_b32 v1, v251 offset:2048
	ds_read_b128 v[150:153], v186 offset:0
	ds_read_b128 v[154:157], v186 offset:1024
	s_nop 2
	v_exp_f32_e32 v226, v210
	v_exp_f32_e32 v227, v211
	v_mfma_f32_16x16x32_f16 v[214:217], v[34:37], v[158:161], v[214:217]
	v_min_f32_e32 v228, s42, v212
	v_exp_f32_e32 v229, v213
	v_mfma_f32_16x16x32_f16 v[214:217], v[38:41], v[162:165], v[214:217]
	v_exp_f32_e32 v228, v228
	v_add_f32_e32 v227, 1.0, v227
	v_mfma_f32_16x16x32_f16 v[214:217], v[42:45], v[166:169], v[214:217]
	v_fma_f32 v230, v228, s41, s41
	v_rcp_f32_e32 v227, v227
	v_mfma_f32_16x16x32_f16 v[214:217], v[46:49], v[170:173], v[214:217]
	v_fma_f32 v230, v226, v230, v230
	v_rcp_f32_e32 v230, v230
	v_mfma_f32_16x16x32_f16 v[218:221], v[18:21], v[158:161], v[218:221]
	v_fma_f32 v226, -v228, v230, v230
	v_fma_f32 v200, v200, v227, v226
	v_mfma_f32_16x16x32_f16 v[218:221], v[14:17], v[162:165], v[218:221]
	v_min_f32_e32 v226, s42, v200
	v_exp_f32_e32 v226, v226
	v_mfma_f32_16x16x32_f16 v[218:221], v[10:13], v[166:169], v[218:221]
	v_add_f32_e32 v227, 1.0, v226
	v_fma_f32 v227, v229, v227, v227
	v_mfma_f32_16x16x32_f16 v[218:221], v[26:29], v[170:173], v[218:221]
	v_rcp_f32_e32 v227, v227
	v_exp_f32_e32 v231, v214
	v_mfma_f32_16x16x32_f16 v[222:225], v[2:5], v[158:161], v[222:225]
	v_exp_f32_e32 v232, v215
	v_fma_f32 v226, -v226, v227, v227
	v_mfma_f32_16x16x32_f16 v[222:225], v[6:9], v[162:165], v[222:225]
	v_min_f32_e32 v233, s42, v216
	v_exp_f32_e32 v234, v217
	v_mfma_f32_16x16x32_f16 v[222:225], v[22:25], v[166:169], v[222:225]
	v_exp_f32_e32 v236, v218
	v_exp_f32_e32 v233, v233
	v_mfma_f32_16x16x32_f16 v[222:225], v[30:33], v[170:173], v[222:225]
	v_add_f32_e32 v232, 1.0, v232
	v_exp_f32_e32 v227, v219
	v_fma_f32 v235, v233, s41, s41
	v_rcp_f32_e32 v232, v232
	v_min_f32_e32 v228, s42, v220
	v_fma_f32 v235, v231, v235, v235
	v_rcp_f32_e32 v235, v235
	v_exp_f32_e32 v229, v221
	v_fma_f32 v231, -v233, v235, v235
	v_fma_f32 v201, v201, v232, v231
	v_exp_f32_e32 v228, v228
	v_min_f32_e32 v231, s42, v201
	v_exp_f32_e32 v231, v231
	v_add_f32_e32 v227, 1.0, v227
	v_add_f32_e32 v232, 1.0, v231
	v_mfma_f32_16x16x32_f16 v[146:149], v[114:117], v[158:161], v[146:149]
	v_fma_f32 v232, v234, v232, v232
	v_fma_f32 v230, v228, s41, s41
	v_rcp_f32_e32 v232, v232
	v_mfma_f32_16x16x32_f16 v[146:149], v[118:121], v[162:165], v[146:149]
	v_fma_f32 v231, -v231, v232, v232
	v_rcp_f32_e32 v227, v227
	v_cvt_pk_f16_f32 v246, v226, v231
	v_exp_f32_e32 v231, v222
	v_fma_f32 v230, v236, v230, v230
	v_exp_f32_e32 v232, v223
	s_waitcnt lgkmcnt(0)
	v_mfma_f32_16x16x32_f16 v[210:213], v[70:73], v[150:153], v[98:101]
	v_min_f32_e32 v233, s42, v224
	v_rcp_f32_e32 v230, v230
	v_exp_f32_e32 v234, v225
	v_mfma_f32_16x16x32_f16 v[214:217], v[74:77], v[150:153], v[102:105]
	v_exp_f32_e32 v233, v233
	v_fma_f32 v236, -v228, v230, v230
	v_add_f32_e32 v232, 1.0, v232
	v_fma_f32 v235, v233, s41, s41
	v_fma_f32 v198, v198, v227, v236
	v_rcp_f32_e32 v232, v232
	v_fma_f32 v235, v231, v235, v235
	v_min_f32_e32 v236, s42, v198
	v_rcp_f32_e32 v235, v235
	s_nop 0
	v_fma_f32 v231, -v233, v235, v235
	v_exp_f32_e32 v236, v236
	v_fma_f32 v199, v199, v232, v231
	v_min_f32_e32 v231, s42, v199
	v_add_f32_e32 v227, 1.0, v236
	v_exp_f32_e32 v231, v231
	v_fma_f32 v227, v229, v227, v227
	v_add_f32_e32 v232, 1.0, v231
	v_rcp_f32_e32 v227, v227
	v_fma_f32 v232, v234, v232, v232
	v_fma_f32 v236, -v236, v227, v227
	v_rcp_f32_e32 v232, v232
	s_nop 0
	v_fma_f32 v231, -v231, v232, v232
	v_cvt_pk_f16_f32 v247, v236, v231
	ds_write_b64 v250, v[246:247] offset:16384
	v_mfma_f32_16x16x32_f16 v[210:213], v[66:69], v[154:157], v[210:213]
	v_mfma_f32_16x16x32_f16 v[214:217], v[78:81], v[154:157], v[214:217]
	s_add_i32 s45, s45, 0x400000
	s_add_i32 s46, s46, 0x10000
	s_waitcnt lgkmcnt(0)
	s_barrier
	ds_read_b128 v[158:161], v248 offset:8192
	ds_read_b128 v[162:165], v248 offset:9216
	ds_read_b128 v[166:169], v249 offset:10240
	ds_read_b128 v[170:173], v249 offset:11264
	v_mfma_f32_16x16x32_f16 v[218:221], v[82:85], v[150:153], v[106:109]
	v_mfma_f32_16x16x32_f16 v[222:225], v[90:93], v[150:153], v[110:113]
	v_mfma_f32_16x16x32_f16 v[218:221], v[86:89], v[154:157], v[218:221]
	v_mfma_f32_16x16x32_f16 v[222:225], v[94:97], v[154:157], v[222:225]
	s_waitcnt lgkmcnt(2)
	v_mfma_f32_16x16x32_f16 v[210:213], v[54:57], v[158:161], v[210:213]
	v_mfma_f32_16x16x32_f16 v[210:213], v[58:61], v[162:165], v[210:213]
	s_waitcnt lgkmcnt(0)
	v_mfma_f32_16x16x32_f16 v[210:213], v[62:65], v[166:169], v[210:213]
	v_mfma_f32_16x16x32_f16 v[210:213], v[50:53], v[170:173], v[210:213]
	s_waitcnt vmcnt(4)
	ds_read_b128 v[150:153], v186 offset:2048
	ds_read_b128 v[154:157], v186 offset:3072
	s_nop 4
	v_exp_f32_e32 v226, v210
	v_exp_f32_e32 v227, v211
	v_mfma_f32_16x16x32_f16 v[214:217], v[34:37], v[158:161], v[214:217]
	v_min_f32_e32 v228, s42, v212
	v_exp_f32_e32 v229, v213
	v_mfma_f32_16x16x32_f16 v[214:217], v[38:41], v[162:165], v[214:217]
	v_exp_f32_e32 v228, v228
	v_add_f32_e32 v227, 1.0, v227
	v_mfma_f32_16x16x32_f16 v[214:217], v[42:45], v[166:169], v[214:217]
	v_fma_f32 v230, v228, s41, s41
	v_rcp_f32_e32 v227, v227
	v_mfma_f32_16x16x32_f16 v[214:217], v[46:49], v[170:173], v[214:217]
	v_fma_f32 v230, v226, v230, v230
	v_rcp_f32_e32 v230, v230
	v_mfma_f32_16x16x32_f16 v[218:221], v[18:21], v[158:161], v[218:221]
	v_fma_f32 v226, -v228, v230, v230
	v_fma_f32 v200, v200, v227, v226
	v_mfma_f32_16x16x32_f16 v[218:221], v[14:17], v[162:165], v[218:221]
	v_min_f32_e32 v226, s42, v200
	v_exp_f32_e32 v226, v226
	v_mfma_f32_16x16x32_f16 v[218:221], v[10:13], v[166:169], v[218:221]
	v_add_f32_e32 v227, 1.0, v226
	v_fma_f32 v227, v229, v227, v227
	v_mfma_f32_16x16x32_f16 v[218:221], v[26:29], v[170:173], v[218:221]
	v_rcp_f32_e32 v227, v227
	v_exp_f32_e32 v231, v214
	v_mfma_f32_16x16x32_f16 v[222:225], v[2:5], v[158:161], v[222:225]
	v_exp_f32_e32 v232, v215
	v_fma_f32 v226, -v226, v227, v227
	v_mfma_f32_16x16x32_f16 v[222:225], v[6:9], v[162:165], v[222:225]
	v_min_f32_e32 v233, s42, v216
	v_exp_f32_e32 v234, v217
	v_mfma_f32_16x16x32_f16 v[222:225], v[22:25], v[166:169], v[222:225]
	v_exp_f32_e32 v236, v218
	v_exp_f32_e32 v233, v233
	v_mfma_f32_16x16x32_f16 v[222:225], v[30:33], v[170:173], v[222:225]
	v_add_f32_e32 v232, 1.0, v232
	v_exp_f32_e32 v227, v219
	v_fma_f32 v235, v233, s41, s41
	v_rcp_f32_e32 v232, v232
	v_min_f32_e32 v228, s42, v220
	v_fma_f32 v235, v231, v235, v235
	v_rcp_f32_e32 v235, v235
	v_exp_f32_e32 v229, v221
	v_fma_f32 v231, -v233, v235, v235
	v_fma_f32 v201, v201, v232, v231
	v_exp_f32_e32 v228, v228
	v_min_f32_e32 v231, s42, v201
	v_exp_f32_e32 v231, v231
	v_add_f32_e32 v227, 1.0, v227
	v_add_f32_e32 v232, 1.0, v231
	v_mfma_f32_16x16x32_f16 v[146:149], v[138:141], v[158:161], v[146:149]
	v_fma_f32 v232, v234, v232, v232
	v_fma_f32 v230, v228, s41, s41
	v_rcp_f32_e32 v232, v232
	v_mfma_f32_16x16x32_f16 v[146:149], v[142:145], v[162:165], v[146:149]
	v_fma_f32 v231, -v231, v232, v232
	v_rcp_f32_e32 v227, v227
	v_cvt_pk_f16_f32 v246, v226, v231
	v_exp_f32_e32 v231, v222
	v_fma_f32 v230, v236, v230, v230
	v_exp_f32_e32 v232, v223
	s_waitcnt lgkmcnt(0)
	v_mfma_f32_16x16x32_f16 v[210:213], v[70:73], v[150:153], v[98:101]
	v_min_f32_e32 v233, s42, v224
	v_rcp_f32_e32 v230, v230
	v_exp_f32_e32 v234, v225
	v_mfma_f32_16x16x32_f16 v[214:217], v[74:77], v[150:153], v[102:105]
	v_exp_f32_e32 v233, v233
	v_fma_f32 v236, -v228, v230, v230
	v_add_f32_e32 v232, 1.0, v232
	v_fma_f32 v235, v233, s41, s41
	v_fma_f32 v198, v198, v227, v236
	v_rcp_f32_e32 v232, v232
	v_fma_f32 v235, v231, v235, v235
	v_min_f32_e32 v236, s42, v198
	v_rcp_f32_e32 v235, v235
	s_nop 0
	v_fma_f32 v231, -v233, v235, v235
	v_exp_f32_e32 v236, v236
	v_fma_f32 v199, v199, v232, v231
	v_min_f32_e32 v231, s42, v199
	v_add_f32_e32 v227, 1.0, v236
	v_exp_f32_e32 v231, v231
	v_fma_f32 v227, v229, v227, v227
	v_add_f32_e32 v232, 1.0, v231
	v_rcp_f32_e32 v227, v227
	v_fma_f32 v232, v234, v232, v232
	v_fma_f32 v236, -v236, v227, v227
	v_rcp_f32_e32 v232, v232
	s_nop 0
	v_fma_f32 v231, -v231, v232, v232
	v_cvt_pk_f16_f32 v247, v236, v231
	ds_write_b64 v250, v[246:247] offset:20480
	v_mfma_f32_16x16x32_f16 v[210:213], v[66:69], v[154:157], v[210:213]
	v_mfma_f32_16x16x32_f16 v[214:217], v[78:81], v[154:157], v[214:217]
	s_waitcnt lgkmcnt(0)
	s_barrier
	ds_read_b128 v[158:161], v248 offset:12288
	ds_read_b128 v[162:165], v248 offset:13312
	ds_read_b128 v[166:169], v249 offset:14336
	ds_read_b128 v[170:173], v249 offset:15360
	v_mfma_f32_16x16x32_f16 v[218:221], v[82:85], v[150:153], v[106:109]
	v_mfma_f32_16x16x32_f16 v[222:225], v[90:93], v[150:153], v[110:113]
	v_mfma_f32_16x16x32_f16 v[218:221], v[86:89], v[154:157], v[218:221]
	v_mfma_f32_16x16x32_f16 v[222:225], v[94:97], v[154:157], v[222:225]
	s_waitcnt lgkmcnt(2)
	v_mfma_f32_16x16x32_f16 v[210:213], v[54:57], v[158:161], v[210:213]
	v_mfma_f32_16x16x32_f16 v[210:213], v[58:61], v[162:165], v[210:213]
	s_waitcnt lgkmcnt(0)
	v_mfma_f32_16x16x32_f16 v[210:213], v[62:65], v[166:169], v[210:213]
	v_mfma_f32_16x16x32_f16 v[210:213], v[50:53], v[170:173], v[210:213]
	s_waitcnt vmcnt(2)
	s_nop 6
	v_exp_f32_e32 v226, v210
	v_exp_f32_e32 v227, v211
	v_mfma_f32_16x16x32_f16 v[214:217], v[34:37], v[158:161], v[214:217]
	v_min_f32_e32 v228, s42, v212
	v_exp_f32_e32 v229, v213
	v_mfma_f32_16x16x32_f16 v[214:217], v[38:41], v[162:165], v[214:217]
	v_exp_f32_e32 v228, v228
	v_add_f32_e32 v227, 1.0, v227
	v_mfma_f32_16x16x32_f16 v[214:217], v[42:45], v[166:169], v[214:217]
	v_fma_f32 v230, v228, s41, s41
	v_rcp_f32_e32 v227, v227
	v_mfma_f32_16x16x32_f16 v[214:217], v[46:49], v[170:173], v[214:217]
	v_fma_f32 v230, v226, v230, v230
	v_rcp_f32_e32 v230, v230
	v_mfma_f32_16x16x32_f16 v[218:221], v[18:21], v[158:161], v[218:221]
	v_fma_f32 v226, -v228, v230, v230
	v_fma_f32 v200, v200, v227, v226
	v_mfma_f32_16x16x32_f16 v[218:221], v[14:17], v[162:165], v[218:221]
	v_min_f32_e32 v226, s42, v200
	v_exp_f32_e32 v226, v226
	v_mfma_f32_16x16x32_f16 v[218:221], v[10:13], v[166:169], v[218:221]
	v_add_f32_e32 v227, 1.0, v226
	v_fma_f32 v227, v229, v227, v227
	v_mfma_f32_16x16x32_f16 v[218:221], v[26:29], v[170:173], v[218:221]
	v_rcp_f32_e32 v227, v227
	v_exp_f32_e32 v231, v214
	v_mfma_f32_16x16x32_f16 v[222:225], v[2:5], v[158:161], v[222:225]
	v_exp_f32_e32 v232, v215
	v_fma_f32 v226, -v226, v227, v227
	v_mfma_f32_16x16x32_f16 v[222:225], v[6:9], v[162:165], v[222:225]
	v_min_f32_e32 v233, s42, v216
	v_exp_f32_e32 v234, v217
	v_mfma_f32_16x16x32_f16 v[222:225], v[22:25], v[166:169], v[222:225]
	v_exp_f32_e32 v236, v218
	v_exp_f32_e32 v233, v233
	v_mfma_f32_16x16x32_f16 v[222:225], v[30:33], v[170:173], v[222:225]
	v_add_f32_e32 v232, 1.0, v232
	v_exp_f32_e32 v227, v219
	v_fma_f32 v235, v233, s41, s41
	v_rcp_f32_e32 v232, v232
	v_min_f32_e32 v228, s42, v220
	v_fma_f32 v235, v231, v235, v235
	v_rcp_f32_e32 v235, v235
	v_exp_f32_e32 v229, v221
	v_fma_f32 v231, -v233, v235, v235
	v_fma_f32 v201, v201, v232, v231
	v_exp_f32_e32 v228, v228
	v_min_f32_e32 v231, s42, v201
	v_exp_f32_e32 v231, v231
	v_add_f32_e32 v227, 1.0, v227
	v_add_f32_e32 v232, 1.0, v231
	v_mfma_f32_16x16x32_f16 v[146:149], v[130:133], v[158:161], v[146:149]
	v_fma_f32 v232, v234, v232, v232
	v_fma_f32 v230, v228, s41, s41
	v_rcp_f32_e32 v232, v232
	v_mfma_f32_16x16x32_f16 v[146:149], v[134:137], v[162:165], v[146:149]
	v_fma_f32 v231, -v231, v232, v232
	v_rcp_f32_e32 v227, v227
	v_cvt_pk_f16_f32 v246, v226, v231
	v_exp_f32_e32 v231, v222
	v_fma_f32 v230, v236, v230, v230
	v_exp_f32_e32 v232, v223
	s_waitcnt lgkmcnt(0)
	v_min_f32_e32 v233, s42, v224
	v_rcp_f32_e32 v230, v230
	v_exp_f32_e32 v234, v225
	v_exp_f32_e32 v233, v233
	v_fma_f32 v236, -v228, v230, v230
	v_add_f32_e32 v232, 1.0, v232
	v_fma_f32 v235, v233, s41, s41
	v_fma_f32 v198, v198, v227, v236
	v_rcp_f32_e32 v232, v232
	v_fma_f32 v235, v231, v235, v235
	v_min_f32_e32 v236, s42, v198
	v_rcp_f32_e32 v235, v235
	s_nop 0
	v_fma_f32 v231, -v233, v235, v235
	v_exp_f32_e32 v236, v236
	v_fma_f32 v199, v199, v232, v231
	v_min_f32_e32 v231, s42, v199
	v_add_f32_e32 v227, 1.0, v236
	v_exp_f32_e32 v231, v231
	v_fma_f32 v227, v229, v227, v227
	v_add_f32_e32 v232, 1.0, v231
	v_rcp_f32_e32 v227, v227
	v_fma_f32 v232, v234, v232, v232
	v_fma_f32 v236, -v236, v227, v227
	v_rcp_f32_e32 v232, v232
	s_nop 0
	v_fma_f32 v231, -v231, v232, v232
	v_cvt_pk_f16_f32 v247, v236, v231
	ds_write_b64 v250, v[246:247] offset:24576
	v_add_u32_e32 v250, 0x4000, v250
	v_add_u32_e32 v248, 0x4000, v248
	v_add_u32_e32 v249, 0x4000, v249
	s_waitcnt lgkmcnt(0)
	s_barrier
	ds_read_b128 v[158:161], v248 offset:0
	ds_read_b128 v[162:165], v248 offset:1024
	s_lshr_b32 s48, s35, 5
	v_and_b32_e32 v211, 15, v0
	v_bfe_u32 v212, v0, 4, 2
	v_and_b32_e32 v213, 31, v0
	v_bfe_u32 v214, v0, 5, 1
	v_add_u32_e32 v214, s48, v214
	s_lshl_b32 s49, s35, 4
	s_addk_i32 s49, 0x2000
	v_lshl_add_u32 v215, v212, 8, s49
	v_lshl_add_u32 v215, v211, 2, v215
	v_lshlrev_b32_e32 v216, 6, v213
	v_lshl_add_u32 v216, v214, 2, v216
	v_mul_u32_u24_e32 v217, 0x110, v214
	v_lshl_add_u32 v217, v213, 2, v217
	v_mul_u32_u24_e32 v218, 0x110, v211
	v_add_u32_e32 v219, 0x4000, v206
	v_add_u32_e32 v220, 0x14000, v206
	v_add_u32_e32 v221, 0x24000, v206
	v_add_u32_e32 v222, s34, v211
	v_lshlrev_b32_e32 v222, 9, v222
	v_add_u32_e32 v222, s35, v222
	v_lshl_add_u32 v222, v212, 4, v222
	s_waitcnt vmcnt(0) lgkmcnt(0)
	v_mfma_f32_16x16x32_f16 v[146:149], v[122:125], v[158:161], v[146:149]
	v_mfma_f32_16x16x32_f16 v[146:149], v[126:129], v[162:165], v[146:149]
	ds_read_b64 v[30:31], v219 offset:0
	ds_read_b64 v[32:33], v219 offset:4096
	ds_read_b64 v[34:35], v219 offset:8192
	ds_read_b64 v[36:37], v219 offset:12288
	ds_read_b64 v[38:39], v219 offset:16384
	ds_read_b64 v[40:41], v219 offset:20480
	ds_read_b64 v[42:43], v219 offset:24576
	ds_read_b64 v[44:45], v219 offset:28672
	s_waitcnt lgkmcnt(4)
	ds_read_b64 v[46:47], v219 offset:32768
	ds_read_b64 v[48:49], v219 offset:36864
	ds_read_b64 v[50:51], v219 offset:40960
	ds_read_b64 v[52:53], v219 offset:45056
	ds_read_b64 v[54:55], v219 offset:49152
	ds_read_b64 v[56:57], v219 offset:53248
	ds_read_b64 v[58:59], v219 offset:57344
	ds_read_b64 v[60:61], v219 offset:61440
	s_waitcnt lgkmcnt(4)
	ds_read_b64 v[62:63], v220 offset:0
	ds_read_b64 v[64:65], v220 offset:4096
	ds_read_b64 v[66:67], v220 offset:8192
	ds_read_b64 v[68:69], v220 offset:12288
	ds_read_b64 v[70:71], v220 offset:16384
	ds_read_b64 v[72:73], v220 offset:20480
	ds_read_b64 v[74:75], v220 offset:24576
	ds_read_b64 v[76:77], v220 offset:28672
	s_waitcnt lgkmcnt(4)
	ds_read_b64 v[78:79], v220 offset:32768
	ds_read_b64 v[80:81], v220 offset:36864
	ds_read_b64 v[82:83], v220 offset:40960
	ds_read_b64 v[84:85], v220 offset:45056
	ds_read_b64 v[86:87], v220 offset:49152
	ds_read_b64 v[88:89], v220 offset:53248
	ds_read_b64 v[90:91], v220 offset:57344
	ds_read_b64 v[92:93], v220 offset:61440
	s_waitcnt lgkmcnt(4)
	ds_read_b64 v[94:95], v221 offset:0
	ds_read_b64 v[96:97], v221 offset:4096
	ds_read_b64 v[98:99], v221 offset:8192
	ds_read_b64 v[100:101], v221 offset:12288
	ds_write2_b32 v215, v146, v147 offset1:16
	ds_write2_b32 v215, v148, v149 offset0:32 offset1:48
	s_waitcnt lgkmcnt(0)
	s_barrier
	ds_read2st64_b32 v[230:231], v216 offset0:32 offset1:48
	ds_read2st64_b32 v[232:233], v216 offset0:40 offset1:56
	v_cmp_gt_u32_e32 vcc, 18, v213
	s_waitcnt vmcnt(0) lgkmcnt(0)
	v_add_f32_e32 v223, v230, v231
	v_add_f32_e32 v224, v232, v233
	v_add_f32_e32 v223, v223, v254
	v_add_f32_e32 v224, v224, v255
	v_max_f32_e32 v223, 0, v223
	v_max_f32_e32 v224, 0, v224
	v_mov_b32_e32 v226, 0xf149f2ca
	v_cndmask_b32_e32 v224, v226, v224, vcc
	v_max_f32_e32 v225, v223, v224
	s_nop 1
	v_max_f32_dpp v226, v225, v225 quad_perm:[1,0,3,2] row_mask:0xf bank_mask:0xf
	s_nop 1
	v_max_f32_dpp v225, v226, v226 quad_perm:[2,3,0,1] row_mask:0xf bank_mask:0xf
	s_nop 1
	v_max_f32_dpp v226, v225, v225 row_half_mirror row_mask:0xf bank_mask:0xf
	s_nop 1
	v_max_f32_dpp v225, v226, v226 row_mirror row_mask:0xf bank_mask:0xf
	ds_swizzle_b32 v226, v225 offset:swizzle(SWAP,16)
	s_waitcnt lgkmcnt(0)
	v_max_f32_e32 v225, v225, v226
	v_sub_f32_e32 v223, v223, v225
	v_sub_f32_e32 v224, v224, v225
	v_mul_f32_e32 v223, 0x3fb8aa3b, v223
	v_mul_f32_e32 v224, 0x3fb8aa3b, v224
	v_exp_f32_e32 v227, v223
	v_exp_f32_e32 v228, v224
	s_nop 0
	v_add_f32_e32 v229, v227, v228
	s_nop 1
	v_add_f32_dpp v226, v229, v229 quad_perm:[1,0,3,2] row_mask:0xf bank_mask:0xf
	s_nop 1
	v_add_f32_dpp v229, v226, v226 quad_perm:[2,3,0,1] row_mask:0xf bank_mask:0xf
	s_nop 1
	v_add_f32_dpp v226, v229, v229 row_half_mirror row_mask:0xf bank_mask:0xf
	s_nop 1
	v_add_f32_dpp v229, v226, v226 row_mirror row_mask:0xf bank_mask:0xf
	ds_swizzle_b32 v226, v229 offset:swizzle(SWAP,16)
	s_waitcnt lgkmcnt(0)
	v_add_f32_e32 v229, v229, v226
	v_rcp_f32_e32 v234, v229
	s_nop 0
	v_mul_f32_e32 v227, v227, v234
	v_mul_f32_e32 v228, v228, v234
	ds_write_b32 v217, v227
	ds_write_b32 v217, v228 offset:128
	s_waitcnt lgkmcnt(0)
	s_barrier
	ds_read_b128 v[102:105], v218 offset:0
	ds_read_b128 v[106:109], v218 offset:16
	ds_read_b128 v[110:113], v218 offset:32
	ds_read_b128 v[114:117], v218 offset:48
	ds_read_b128 v[118:121], v218 offset:64
	ds_read_b128 v[122:125], v218 offset:80
	ds_read_b128 v[126:129], v218 offset:96
	ds_read_b128 v[130:133], v218 offset:112
	ds_read_b128 v[134:137], v218 offset:128
	ds_read_b128 v[138:141], v218 offset:144
	ds_read_b128 v[142:145], v218 offset:160
	ds_read_b128 v[146:149], v218 offset:176
	ds_read_b128 v[150:153], v218 offset:192
	v_mov_b32_e32 v154, 0
	v_mov_b32_e32 v155, 0
	v_mov_b32_e32 v156, 0
	v_mov_b32_e32 v157, 0
	s_waitcnt vmcnt(0) lgkmcnt(0)
	v_fma_mix_f32 v154, v174, v102, v154 op_sel_hi:[1,0,0]
	v_fma_mix_f32 v155, v174, v102, v155 op_sel:[1,0,0] op_sel_hi:[1,0,0]
	v_fma_mix_f32 v156, v175, v102, v156 op_sel_hi:[1,0,0]
	v_fma_mix_f32 v157, v175, v102, v157 op_sel:[1,0,0] op_sel_hi:[1,0,0]
	v_fma_mix_f32 v154, v176, v103, v154 op_sel_hi:[1,0,0]
	v_fma_mix_f32 v155, v176, v103, v155 op_sel:[1,0,0] op_sel_hi:[1,0,0]
	v_fma_mix_f32 v156, v177, v103, v156 op_sel_hi:[1,0,0]
	v_fma_mix_f32 v157, v177, v103, v157 op_sel:[1,0,0] op_sel_hi:[1,0,0]
	v_fma_mix_f32 v154, v178, v104, v154 op_sel_hi:[1,0,0]
	v_fma_mix_f32 v155, v178, v104, v155 op_sel:[1,0,0] op_sel_hi:[1,0,0]
	v_fma_mix_f32 v156, v179, v104, v156 op_sel_hi:[1,0,0]
	v_fma_mix_f32 v157, v179, v104, v157 op_sel:[1,0,0] op_sel_hi:[1,0,0]
	v_fma_mix_f32 v154, v180, v105, v154 op_sel_hi:[1,0,0]
	v_fma_mix_f32 v155, v180, v105, v155 op_sel:[1,0,0] op_sel_hi:[1,0,0]
	v_fma_mix_f32 v156, v181, v105, v156 op_sel_hi:[1,0,0]
	v_fma_mix_f32 v157, v181, v105, v157 op_sel:[1,0,0] op_sel_hi:[1,0,0]
	v_fma_mix_f32 v154, v182, v106, v154 op_sel_hi:[1,0,0]
	v_fma_mix_f32 v155, v182, v106, v155 op_sel:[1,0,0] op_sel_hi:[1,0,0]
	v_fma_mix_f32 v156, v183, v106, v156 op_sel_hi:[1,0,0]
	v_fma_mix_f32 v157, v183, v106, v157 op_sel:[1,0,0] op_sel_hi:[1,0,0]
	v_fma_mix_f32 v154, v184, v107, v154 op_sel_hi:[1,0,0]
	v_fma_mix_f32 v155, v184, v107, v155 op_sel:[1,0,0] op_sel_hi:[1,0,0]
	v_fma_mix_f32 v156, v185, v107, v156 op_sel_hi:[1,0,0]
	v_fma_mix_f32 v157, v185, v107, v157 op_sel:[1,0,0] op_sel_hi:[1,0,0]
	v_fma_mix_f32 v154, v237, v108, v154 op_sel_hi:[1,0,0]
	v_fma_mix_f32 v155, v237, v108, v155 op_sel:[1,0,0] op_sel_hi:[1,0,0]
	v_fma_mix_f32 v156, v238, v108, v156 op_sel_hi:[1,0,0]
	v_fma_mix_f32 v157, v238, v108, v157 op_sel:[1,0,0] op_sel_hi:[1,0,0]
	v_fma_mix_f32 v154, v239, v109, v154 op_sel_hi:[1,0,0]
	v_fma_mix_f32 v155, v239, v109, v155 op_sel:[1,0,0] op_sel_hi:[1,0,0]
	v_fma_mix_f32 v156, v240, v109, v156 op_sel_hi:[1,0,0]
	v_fma_mix_f32 v157, v240, v109, v157 op_sel:[1,0,0] op_sel_hi:[1,0,0]
	v_fma_mix_f32 v154, v241, v110, v154 op_sel_hi:[1,0,0]
	v_fma_mix_f32 v155, v241, v110, v155 op_sel:[1,0,0] op_sel_hi:[1,0,0]
	v_fma_mix_f32 v156, v242, v110, v156 op_sel_hi:[1,0,0]
	v_fma_mix_f32 v157, v242, v110, v157 op_sel:[1,0,0] op_sel_hi:[1,0,0]
	v_fma_mix_f32 v154, v243, v111, v154 op_sel_hi:[1,0,0]
	v_fma_mix_f32 v155, v243, v111, v155 op_sel:[1,0,0] op_sel_hi:[1,0,0]
	v_fma_mix_f32 v156, v244, v111, v156 op_sel_hi:[1,0,0]
	v_fma_mix_f32 v157, v244, v111, v157 op_sel:[1,0,0] op_sel_hi:[1,0,0]
	v_fma_mix_f32 v154, v245, v112, v154 op_sel_hi:[1,0,0]
	v_fma_mix_f32 v155, v245, v112, v155 op_sel:[1,0,0] op_sel_hi:[1,0,0]
	v_fma_mix_f32 v156, v187, v112, v156 op_sel_hi:[1,0,0]
	v_fma_mix_f32 v157, v187, v112, v157 op_sel:[1,0,0] op_sel_hi:[1,0,0]
	v_fma_mix_f32 v154, v188, v113, v154 op_sel_hi:[1,0,0]
	v_fma_mix_f32 v155, v188, v113, v155 op_sel:[1,0,0] op_sel_hi:[1,0,0]
	v_fma_mix_f32 v156, v202, v113, v156 op_sel_hi:[1,0,0]
	v_fma_mix_f32 v157, v202, v113, v157 op_sel:[1,0,0] op_sel_hi:[1,0,0]
	v_fma_mix_f32 v154, v203, v114, v154 op_sel_hi:[1,0,0]
	v_fma_mix_f32 v155, v203, v114, v155 op_sel:[1,0,0] op_sel_hi:[1,0,0]
	v_fma_mix_f32 v156, v204, v114, v156 op_sel_hi:[1,0,0]
	v_fma_mix_f32 v157, v204, v114, v157 op_sel:[1,0,0] op_sel_hi:[1,0,0]
	v_fma_mix_f32 v154, v205, v115, v154 op_sel_hi:[1,0,0]
	v_fma_mix_f32 v155, v205, v115, v155 op_sel:[1,0,0] op_sel_hi:[1,0,0]
	v_fma_mix_f32 v156, v207, v115, v156 op_sel_hi:[1,0,0]
	v_fma_mix_f32 v157, v207, v115, v157 op_sel:[1,0,0] op_sel_hi:[1,0,0]
	v_fma_mix_f32 v154, v30, v116, v154 op_sel_hi:[1,0,0]
	v_fma_mix_f32 v155, v30, v116, v155 op_sel:[1,0,0] op_sel_hi:[1,0,0]
	v_fma_mix_f32 v156, v31, v116, v156 op_sel_hi:[1,0,0]
	v_fma_mix_f32 v157, v31, v116, v157 op_sel:[1,0,0] op_sel_hi:[1,0,0]
	v_fma_mix_f32 v154, v32, v117, v154 op_sel_hi:[1,0,0]
	v_fma_mix_f32 v155, v32, v117, v155 op_sel:[1,0,0] op_sel_hi:[1,0,0]
	v_fma_mix_f32 v156, v33, v117, v156 op_sel_hi:[1,0,0]
	v_fma_mix_f32 v157, v33, v117, v157 op_sel:[1,0,0] op_sel_hi:[1,0,0]
	v_fma_mix_f32 v154, v34, v118, v154 op_sel_hi:[1,0,0]
	v_fma_mix_f32 v155, v34, v118, v155 op_sel:[1,0,0] op_sel_hi:[1,0,0]
	v_fma_mix_f32 v156, v35, v118, v156 op_sel_hi:[1,0,0]
	v_fma_mix_f32 v157, v35, v118, v157 op_sel:[1,0,0] op_sel_hi:[1,0,0]
	v_fma_mix_f32 v154, v36, v119, v154 op_sel_hi:[1,0,0]
	v_fma_mix_f32 v155, v36, v119, v155 op_sel:[1,0,0] op_sel_hi:[1,0,0]
	v_fma_mix_f32 v156, v37, v119, v156 op_sel_hi:[1,0,0]
	v_fma_mix_f32 v157, v37, v119, v157 op_sel:[1,0,0] op_sel_hi:[1,0,0]
	v_fma_mix_f32 v154, v38, v120, v154 op_sel_hi:[1,0,0]
	v_fma_mix_f32 v155, v38, v120, v155 op_sel:[1,0,0] op_sel_hi:[1,0,0]
	v_fma_mix_f32 v156, v39, v120, v156 op_sel_hi:[1,0,0]
	v_fma_mix_f32 v157, v39, v120, v157 op_sel:[1,0,0] op_sel_hi:[1,0,0]
	v_fma_mix_f32 v154, v40, v121, v154 op_sel_hi:[1,0,0]
	v_fma_mix_f32 v155, v40, v121, v155 op_sel:[1,0,0] op_sel_hi:[1,0,0]
	v_fma_mix_f32 v156, v41, v121, v156 op_sel_hi:[1,0,0]
	v_fma_mix_f32 v157, v41, v121, v157 op_sel:[1,0,0] op_sel_hi:[1,0,0]
	v_fma_mix_f32 v154, v42, v122, v154 op_sel_hi:[1,0,0]
	v_fma_mix_f32 v155, v42, v122, v155 op_sel:[1,0,0] op_sel_hi:[1,0,0]
	v_fma_mix_f32 v156, v43, v122, v156 op_sel_hi:[1,0,0]
	v_fma_mix_f32 v157, v43, v122, v157 op_sel:[1,0,0] op_sel_hi:[1,0,0]
	v_fma_mix_f32 v154, v44, v123, v154 op_sel_hi:[1,0,0]
	v_fma_mix_f32 v155, v44, v123, v155 op_sel:[1,0,0] op_sel_hi:[1,0,0]
	v_fma_mix_f32 v156, v45, v123, v156 op_sel_hi:[1,0,0]
	v_fma_mix_f32 v157, v45, v123, v157 op_sel:[1,0,0] op_sel_hi:[1,0,0]
	v_fma_mix_f32 v154, v46, v124, v154 op_sel_hi:[1,0,0]
	v_fma_mix_f32 v155, v46, v124, v155 op_sel:[1,0,0] op_sel_hi:[1,0,0]
	v_fma_mix_f32 v156, v47, v124, v156 op_sel_hi:[1,0,0]
	v_fma_mix_f32 v157, v47, v124, v157 op_sel:[1,0,0] op_sel_hi:[1,0,0]
	v_fma_mix_f32 v154, v48, v125, v154 op_sel_hi:[1,0,0]
	v_fma_mix_f32 v155, v48, v125, v155 op_sel:[1,0,0] op_sel_hi:[1,0,0]
	v_fma_mix_f32 v156, v49, v125, v156 op_sel_hi:[1,0,0]
	v_fma_mix_f32 v157, v49, v125, v157 op_sel:[1,0,0] op_sel_hi:[1,0,0]
	v_fma_mix_f32 v154, v50, v126, v154 op_sel_hi:[1,0,0]
	v_fma_mix_f32 v155, v50, v126, v155 op_sel:[1,0,0] op_sel_hi:[1,0,0]
	v_fma_mix_f32 v156, v51, v126, v156 op_sel_hi:[1,0,0]
	v_fma_mix_f32 v157, v51, v126, v157 op_sel:[1,0,0] op_sel_hi:[1,0,0]
	v_fma_mix_f32 v154, v52, v127, v154 op_sel_hi:[1,0,0]
	v_fma_mix_f32 v155, v52, v127, v155 op_sel:[1,0,0] op_sel_hi:[1,0,0]
	v_fma_mix_f32 v156, v53, v127, v156 op_sel_hi:[1,0,0]
	v_fma_mix_f32 v157, v53, v127, v157 op_sel:[1,0,0] op_sel_hi:[1,0,0]
	v_fma_mix_f32 v154, v54, v128, v154 op_sel_hi:[1,0,0]
	v_fma_mix_f32 v155, v54, v128, v155 op_sel:[1,0,0] op_sel_hi:[1,0,0]
	v_fma_mix_f32 v156, v55, v128, v156 op_sel_hi:[1,0,0]
	v_fma_mix_f32 v157, v55, v128, v157 op_sel:[1,0,0] op_sel_hi:[1,0,0]
	v_fma_mix_f32 v154, v56, v129, v154 op_sel_hi:[1,0,0]
	v_fma_mix_f32 v155, v56, v129, v155 op_sel:[1,0,0] op_sel_hi:[1,0,0]
	v_fma_mix_f32 v156, v57, v129, v156 op_sel_hi:[1,0,0]
	v_fma_mix_f32 v157, v57, v129, v157 op_sel:[1,0,0] op_sel_hi:[1,0,0]
	v_fma_mix_f32 v154, v58, v130, v154 op_sel_hi:[1,0,0]
	v_fma_mix_f32 v155, v58, v130, v155 op_sel:[1,0,0] op_sel_hi:[1,0,0]
	v_fma_mix_f32 v156, v59, v130, v156 op_sel_hi:[1,0,0]
	v_fma_mix_f32 v157, v59, v130, v157 op_sel:[1,0,0] op_sel_hi:[1,0,0]
	v_fma_mix_f32 v154, v60, v131, v154 op_sel_hi:[1,0,0]
	v_fma_mix_f32 v155, v60, v131, v155 op_sel:[1,0,0] op_sel_hi:[1,0,0]
	v_fma_mix_f32 v156, v61, v131, v156 op_sel_hi:[1,0,0]
	v_fma_mix_f32 v157, v61, v131, v157 op_sel:[1,0,0] op_sel_hi:[1,0,0]
	v_fma_mix_f32 v154, v62, v132, v154 op_sel_hi:[1,0,0]
	v_fma_mix_f32 v155, v62, v132, v155 op_sel:[1,0,0] op_sel_hi:[1,0,0]
	v_fma_mix_f32 v156, v63, v132, v156 op_sel_hi:[1,0,0]
	v_fma_mix_f32 v157, v63, v132, v157 op_sel:[1,0,0] op_sel_hi:[1,0,0]
	v_fma_mix_f32 v154, v64, v133, v154 op_sel_hi:[1,0,0]
	v_fma_mix_f32 v155, v64, v133, v155 op_sel:[1,0,0] op_sel_hi:[1,0,0]
	v_fma_mix_f32 v156, v65, v133, v156 op_sel_hi:[1,0,0]
	v_fma_mix_f32 v157, v65, v133, v157 op_sel:[1,0,0] op_sel_hi:[1,0,0]
	v_fma_mix_f32 v154, v66, v134, v154 op_sel_hi:[1,0,0]
	v_fma_mix_f32 v155, v66, v134, v155 op_sel:[1,0,0] op_sel_hi:[1,0,0]
	v_fma_mix_f32 v156, v67, v134, v156 op_sel_hi:[1,0,0]
	v_fma_mix_f32 v157, v67, v134, v157 op_sel:[1,0,0] op_sel_hi:[1,0,0]
	v_fma_mix_f32 v154, v68, v135, v154 op_sel_hi:[1,0,0]
	v_fma_mix_f32 v155, v68, v135, v155 op_sel:[1,0,0] op_sel_hi:[1,0,0]
	v_fma_mix_f32 v156, v69, v135, v156 op_sel_hi:[1,0,0]
	v_fma_mix_f32 v157, v69, v135, v157 op_sel:[1,0,0] op_sel_hi:[1,0,0]
	v_fma_mix_f32 v154, v70, v136, v154 op_sel_hi:[1,0,0]
	v_fma_mix_f32 v155, v70, v136, v155 op_sel:[1,0,0] op_sel_hi:[1,0,0]
	v_fma_mix_f32 v156, v71, v136, v156 op_sel_hi:[1,0,0]
	v_fma_mix_f32 v157, v71, v136, v157 op_sel:[1,0,0] op_sel_hi:[1,0,0]
	v_fma_mix_f32 v154, v72, v137, v154 op_sel_hi:[1,0,0]
	v_fma_mix_f32 v155, v72, v137, v155 op_sel:[1,0,0] op_sel_hi:[1,0,0]
	v_fma_mix_f32 v156, v73, v137, v156 op_sel_hi:[1,0,0]
	v_fma_mix_f32 v157, v73, v137, v157 op_sel:[1,0,0] op_sel_hi:[1,0,0]
	v_fma_mix_f32 v154, v74, v138, v154 op_sel_hi:[1,0,0]
	v_fma_mix_f32 v155, v74, v138, v155 op_sel:[1,0,0] op_sel_hi:[1,0,0]
	v_fma_mix_f32 v156, v75, v138, v156 op_sel_hi:[1,0,0]
	v_fma_mix_f32 v157, v75, v138, v157 op_sel:[1,0,0] op_sel_hi:[1,0,0]
	v_fma_mix_f32 v154, v76, v139, v154 op_sel_hi:[1,0,0]
	v_fma_mix_f32 v155, v76, v139, v155 op_sel:[1,0,0] op_sel_hi:[1,0,0]
	v_fma_mix_f32 v156, v77, v139, v156 op_sel_hi:[1,0,0]
	v_fma_mix_f32 v157, v77, v139, v157 op_sel:[1,0,0] op_sel_hi:[1,0,0]
	v_fma_mix_f32 v154, v78, v140, v154 op_sel_hi:[1,0,0]
	v_fma_mix_f32 v155, v78, v140, v155 op_sel:[1,0,0] op_sel_hi:[1,0,0]
	v_fma_mix_f32 v156, v79, v140, v156 op_sel_hi:[1,0,0]
	v_fma_mix_f32 v157, v79, v140, v157 op_sel:[1,0,0] op_sel_hi:[1,0,0]
	v_fma_mix_f32 v154, v80, v141, v154 op_sel_hi:[1,0,0]
	v_fma_mix_f32 v155, v80, v141, v155 op_sel:[1,0,0] op_sel_hi:[1,0,0]
	v_fma_mix_f32 v156, v81, v141, v156 op_sel_hi:[1,0,0]
	v_fma_mix_f32 v157, v81, v141, v157 op_sel:[1,0,0] op_sel_hi:[1,0,0]
	v_fma_mix_f32 v154, v82, v142, v154 op_sel_hi:[1,0,0]
	v_fma_mix_f32 v155, v82, v142, v155 op_sel:[1,0,0] op_sel_hi:[1,0,0]
	v_fma_mix_f32 v156, v83, v142, v156 op_sel_hi:[1,0,0]
	v_fma_mix_f32 v157, v83, v142, v157 op_sel:[1,0,0] op_sel_hi:[1,0,0]
	v_fma_mix_f32 v154, v84, v143, v154 op_sel_hi:[1,0,0]
	v_fma_mix_f32 v155, v84, v143, v155 op_sel:[1,0,0] op_sel_hi:[1,0,0]
	v_fma_mix_f32 v156, v85, v143, v156 op_sel_hi:[1,0,0]
	v_fma_mix_f32 v157, v85, v143, v157 op_sel:[1,0,0] op_sel_hi:[1,0,0]
	v_fma_mix_f32 v154, v86, v144, v154 op_sel_hi:[1,0,0]
	v_fma_mix_f32 v155, v86, v144, v155 op_sel:[1,0,0] op_sel_hi:[1,0,0]
	v_fma_mix_f32 v156, v87, v144, v156 op_sel_hi:[1,0,0]
	v_fma_mix_f32 v157, v87, v144, v157 op_sel:[1,0,0] op_sel_hi:[1,0,0]
	v_fma_mix_f32 v154, v88, v145, v154 op_sel_hi:[1,0,0]
	v_fma_mix_f32 v155, v88, v145, v155 op_sel:[1,0,0] op_sel_hi:[1,0,0]
	v_fma_mix_f32 v156, v89, v145, v156 op_sel_hi:[1,0,0]
	v_fma_mix_f32 v157, v89, v145, v157 op_sel:[1,0,0] op_sel_hi:[1,0,0]
	v_fma_mix_f32 v154, v90, v146, v154 op_sel_hi:[1,0,0]
	v_fma_mix_f32 v155, v90, v146, v155 op_sel:[1,0,0] op_sel_hi:[1,0,0]
	v_fma_mix_f32 v156, v91, v146, v156 op_sel_hi:[1,0,0]
	v_fma_mix_f32 v157, v91, v146, v157 op_sel:[1,0,0] op_sel_hi:[1,0,0]
	v_fma_mix_f32 v154, v92, v147, v154 op_sel_hi:[1,0,0]
	v_fma_mix_f32 v155, v92, v147, v155 op_sel:[1,0,0] op_sel_hi:[1,0,0]
	v_fma_mix_f32 v156, v93, v147, v156 op_sel_hi:[1,0,0]
	v_fma_mix_f32 v157, v93, v147, v157 op_sel:[1,0,0] op_sel_hi:[1,0,0]
	v_fma_mix_f32 v154, v94, v148, v154 op_sel_hi:[1,0,0]
	v_fma_mix_f32 v155, v94, v148, v155 op_sel:[1,0,0] op_sel_hi:[1,0,0]
	v_fma_mix_f32 v156, v95, v148, v156 op_sel_hi:[1,0,0]
	v_fma_mix_f32 v157, v95, v148, v157 op_sel:[1,0,0] op_sel_hi:[1,0,0]
	v_fma_mix_f32 v154, v96, v149, v154 op_sel_hi:[1,0,0]
	v_fma_mix_f32 v155, v96, v149, v155 op_sel:[1,0,0] op_sel_hi:[1,0,0]
	v_fma_mix_f32 v156, v97, v149, v156 op_sel_hi:[1,0,0]
	v_fma_mix_f32 v157, v97, v149, v157 op_sel:[1,0,0] op_sel_hi:[1,0,0]
	v_fma_mix_f32 v154, v98, v150, v154 op_sel_hi:[1,0,0]
	v_fma_mix_f32 v155, v98, v150, v155 op_sel:[1,0,0] op_sel_hi:[1,0,0]
	v_fma_mix_f32 v156, v99, v150, v156 op_sel_hi:[1,0,0]
	v_fma_mix_f32 v157, v99, v150, v157 op_sel:[1,0,0] op_sel_hi:[1,0,0]
	v_fma_mix_f32 v154, v100, v151, v154 op_sel_hi:[1,0,0]
	v_fma_mix_f32 v155, v100, v151, v155 op_sel:[1,0,0] op_sel_hi:[1,0,0]
	v_fma_mix_f32 v156, v101, v151, v156 op_sel_hi:[1,0,0]
	v_fma_mix_f32 v157, v101, v151, v157 op_sel:[1,0,0] op_sel_hi:[1,0,0]
	global_store_dwordx4 v222, v[154:157], s[8:9]
	s_endpgm
